# v100 with the 100 redundant s_waitcnt lgkmcnt lines inside the MFMA blocks removed (32 MFMAs strictly consecutive)
# baseline (speedup 1.0000x reference)
.LBB0_114:
	ds_read_b128 v[130:133], v220
	ds_read_b128 v[134:137], v220 offset:1024
	ds_read_b128 v[138:141], v220 offset:2048
	ds_read_b128 v[142:145], v220 offset:3072
	ds_read_b128 v[146:149], v221
	ds_read_b128 v[150:153], v221 offset:1024
	ds_read_b128 v[154:157], v221 offset:2048
	ds_read_b128 v[158:161], v221 offset:3072
	s_add_i32 s46, s64, 0xfff80080
	s_cmp_eq_u32 s84, 28
	s_cselect_b32 s87, s62, s46
	s_cselect_b32 s86, s63, s65
	s_or_b32 s85, s87, 0x80
	s_mov_b32 m0, s93
	ds_read_b128 v[162:165], v222
	ds_read_b128 v[166:169], v222 offset:1024
	ds_read_b128 v[170:173], v222 offset:2048
	ds_read_b128 v[174:177], v222 offset:3072
	ds_read_b128 v[178:181], v222 offset:4096
	ds_read_b128 v[182:185], v222 offset:5120
	ds_read_b128 v[186:189], v222 offset:6144
	ds_read_b128 v[212:215], v222 offset:7168
	buffer_load_dwordx4 v1, s[40:43], s64 offen lds
	s_mov_b32 m0, s94
	s_nop 0
	buffer_load_dwordx4 v216, s[40:43], s64 offen lds
	s_waitcnt vmcnt(8)
	s_waitcnt lgkmcnt(0)
	s_barrier
	v_mfma_f32_16x16x32_bf16 v[126:129], v[130:133], v[162:165], v[126:129]
	v_mfma_f32_16x16x32_bf16 v[126:129], v[134:137], v[166:169], v[126:129]
	v_mfma_f32_16x16x32_bf16 v[122:125], v[142:145], v[166:169], v[122:125]
	v_mfma_f32_16x16x32_bf16 v[122:125], v[138:141], v[162:165], v[122:125]
	v_mfma_f32_16x16x32_bf16 v[106:109], v[138:141], v[170:173], v[106:109]
	v_mfma_f32_16x16x32_bf16 v[106:109], v[142:145], v[174:177], v[106:109]
	v_mfma_f32_16x16x32_bf16 v[114:117], v[134:137], v[174:177], v[114:117]
	v_mfma_f32_16x16x32_bf16 v[114:117], v[130:133], v[170:173], v[114:117]
	v_mfma_f32_16x16x32_bf16 v[102:105], v[130:133], v[178:181], v[102:105]
	v_mfma_f32_16x16x32_bf16 v[102:105], v[134:137], v[182:185], v[102:105]
	v_mfma_f32_16x16x32_bf16 v[94:97], v[142:145], v[182:185], v[94:97]
	v_mfma_f32_16x16x32_bf16 v[94:97], v[138:141], v[178:181], v[94:97]
	v_mfma_f32_16x16x32_bf16 v[78:81], v[138:141], v[186:189], v[78:81]
	v_mfma_f32_16x16x32_bf16 v[78:81], v[142:145], v[212:215], v[78:81]
	v_mfma_f32_16x16x32_bf16 v[86:89], v[134:137], v[212:215], v[86:89]
	v_mfma_f32_16x16x32_bf16 v[86:89], v[130:133], v[186:189], v[86:89]
	v_mfma_f32_16x16x32_bf16 v[118:121], v[146:149], v[162:165], v[118:121]
	v_mfma_f32_16x16x32_bf16 v[118:121], v[150:153], v[166:169], v[118:121]
	v_mfma_f32_16x16x32_bf16 v[110:113], v[158:161], v[166:169], v[110:113]
	v_mfma_f32_16x16x32_bf16 v[110:113], v[154:157], v[162:165], v[110:113]
	v_mfma_f32_16x16x32_bf16 v[90:93], v[154:157], v[170:173], v[90:93]
	v_mfma_f32_16x16x32_bf16 v[90:93], v[158:161], v[174:177], v[90:93]
	v_mfma_f32_16x16x32_bf16 v[98:101], v[150:153], v[174:177], v[98:101]
	v_mfma_f32_16x16x32_bf16 v[98:101], v[146:149], v[170:173], v[98:101]
	v_mfma_f32_16x16x32_bf16 v[82:85], v[146:149], v[178:181], v[82:85]
	v_mfma_f32_16x16x32_bf16 v[82:85], v[150:153], v[182:185], v[82:85]
	v_mfma_f32_16x16x32_bf16 v[74:77], v[158:161], v[182:185], v[74:77]
	v_mfma_f32_16x16x32_bf16 v[74:77], v[154:157], v[178:181], v[74:77]
	v_mfma_f32_16x16x32_bf16 v[66:69], v[154:157], v[186:189], v[66:69]
	v_mfma_f32_16x16x32_bf16 v[66:69], v[158:161], v[212:215], v[66:69]
	v_mfma_f32_16x16x32_bf16 v[70:73], v[150:153], v[212:215], v[70:73]
	v_mfma_f32_16x16x32_bf16 v[70:73], v[146:149], v[186:189], v[70:73]
	s_barrier
	s_mov_b32 m0, s69
	s_mov_b32 s46, s42
	s_mov_b32 s47, s43
	ds_read_b128 v[162:165], v222 offset:16384
	ds_read_b128 v[166:169], v222 offset:17408
	ds_read_b128 v[170:173], v222 offset:18432
	ds_read_b128 v[174:177], v222 offset:19456
	ds_read_b128 v[178:181], v222 offset:20480
	ds_read_b128 v[182:185], v222 offset:21504
	ds_read_b128 v[186:189], v222 offset:22528
	ds_read_b128 v[212:215], v222 offset:23552
	buffer_load_dwordx4 v191, s[44:47], s86 offen lds
	s_mov_b32 m0, s70
	s_add_i32 s88, s86, 0x80000
	buffer_load_dwordx4 v217, s[44:47], s86 offen lds
	s_mov_b32 m0, s71
	s_nop 0
	buffer_load_dwordx4 v191, s[44:47], s88 offen lds
	s_mov_b32 m0, s72
	s_nop 0
	buffer_load_dwordx4 v217, s[44:47], s88 offen lds
	s_mov_b32 m0, s68
	s_nop 0
	buffer_load_dwordx4 v1, s[40:43], s87 offen lds
	s_mov_b32 m0, s73
	s_nop 0
	buffer_load_dwordx4 v216, s[40:43], s87 offen lds
	s_waitcnt vmcnt(8)
	s_waitcnt lgkmcnt(0)
	s_barrier
	v_mfma_f32_16x16x32_bf16 v[62:65], v[130:133], v[162:165], v[62:65]
	v_mfma_f32_16x16x32_bf16 v[62:65], v[134:137], v[166:169], v[62:65]
	v_mfma_f32_16x16x32_bf16 v[58:61], v[142:145], v[166:169], v[58:61]
	v_mfma_f32_16x16x32_bf16 v[58:61], v[138:141], v[162:165], v[58:61]
	v_mfma_f32_16x16x32_bf16 v[46:49], v[138:141], v[170:173], v[46:49]
	v_mfma_f32_16x16x32_bf16 v[46:49], v[142:145], v[174:177], v[46:49]
	v_mfma_f32_16x16x32_bf16 v[54:57], v[134:137], v[174:177], v[54:57]
	v_mfma_f32_16x16x32_bf16 v[54:57], v[130:133], v[170:173], v[54:57]
	v_mfma_f32_16x16x32_bf16 v[38:41], v[130:133], v[178:181], v[38:41]
	v_mfma_f32_16x16x32_bf16 v[38:41], v[134:137], v[182:185], v[38:41]
	v_mfma_f32_16x16x32_bf16 v[30:33], v[142:145], v[182:185], v[30:33]
	v_mfma_f32_16x16x32_bf16 v[30:33], v[138:141], v[178:181], v[30:33]
	v_mfma_f32_16x16x32_bf16 v[14:17], v[138:141], v[186:189], v[14:17]
	v_mfma_f32_16x16x32_bf16 v[14:17], v[142:145], v[212:215], v[14:17]
	v_mfma_f32_16x16x32_bf16 v[22:25], v[134:137], v[212:215], v[22:25]
	v_mfma_f32_16x16x32_bf16 v[22:25], v[130:133], v[186:189], v[22:25]
	v_mfma_f32_16x16x32_bf16 v[50:53], v[146:149], v[162:165], v[50:53]
	v_mfma_f32_16x16x32_bf16 v[50:53], v[150:153], v[166:169], v[50:53]
	v_mfma_f32_16x16x32_bf16 v[42:45], v[158:161], v[166:169], v[42:45]
	v_mfma_f32_16x16x32_bf16 v[42:45], v[154:157], v[162:165], v[42:45]
	v_mfma_f32_16x16x32_bf16 v[26:29], v[154:157], v[170:173], v[26:29]
	v_mfma_f32_16x16x32_bf16 v[26:29], v[158:161], v[174:177], v[26:29]
	v_mfma_f32_16x16x32_bf16 v[34:37], v[150:153], v[174:177], v[34:37]
	v_mfma_f32_16x16x32_bf16 v[34:37], v[146:149], v[170:173], v[34:37]
	v_mfma_f32_16x16x32_bf16 v[18:21], v[146:149], v[178:181], v[18:21]
	v_mfma_f32_16x16x32_bf16 v[18:21], v[150:153], v[182:185], v[18:21]
	v_mfma_f32_16x16x32_bf16 v[10:13], v[158:161], v[182:185], v[10:13]
	v_mfma_f32_16x16x32_bf16 v[10:13], v[154:157], v[178:181], v[10:13]
	v_mfma_f32_16x16x32_bf16 v[2:5], v[154:157], v[186:189], v[2:5]
	v_mfma_f32_16x16x32_bf16 v[2:5], v[158:161], v[212:215], v[2:5]
	v_mfma_f32_16x16x32_bf16 v[6:9], v[150:153], v[212:215], v[6:9]
	v_mfma_f32_16x16x32_bf16 v[6:9], v[146:149], v[186:189], v[6:9]
	s_barrier
	ds_read_b128 v[130:133], v223
	ds_read_b128 v[134:137], v223 offset:1024
	ds_read_b128 v[138:141], v223 offset:2048
	ds_read_b128 v[142:145], v223 offset:3072
	ds_read_b128 v[146:149], v224
	ds_read_b128 v[150:153], v224 offset:1024
	ds_read_b128 v[154:157], v224 offset:2048
	ds_read_b128 v[158:161], v224 offset:3072
	s_add_i32 s87, s87, 0x80000
	s_mov_b32 m0, s74
	ds_read_b128 v[162:165], v222 offset:32768
	ds_read_b128 v[166:169], v222 offset:33792
	ds_read_b128 v[170:173], v222 offset:34816
	ds_read_b128 v[174:177], v222 offset:35840
	ds_read_b128 v[178:181], v222 offset:36864
	ds_read_b128 v[182:185], v222 offset:37888
	ds_read_b128 v[186:189], v222 offset:38912
	ds_read_b128 v[212:215], v222 offset:39936
	buffer_load_dwordx4 v1, s[40:43], s87 offen lds
	s_mov_b32 m0, s75
	s_nop 0
	buffer_load_dwordx4 v216, s[40:43], s87 offen lds
	s_waitcnt vmcnt(8)
	s_waitcnt lgkmcnt(0)
	s_barrier
	v_mfma_f32_16x16x32_bf16 v[126:129], v[130:133], v[162:165], v[126:129]
	v_mfma_f32_16x16x32_bf16 v[126:129], v[134:137], v[166:169], v[126:129]
	v_mfma_f32_16x16x32_bf16 v[122:125], v[142:145], v[166:169], v[122:125]
	v_mfma_f32_16x16x32_bf16 v[122:125], v[138:141], v[162:165], v[122:125]
	v_mfma_f32_16x16x32_bf16 v[106:109], v[138:141], v[170:173], v[106:109]
	v_mfma_f32_16x16x32_bf16 v[106:109], v[142:145], v[174:177], v[106:109]
	v_mfma_f32_16x16x32_bf16 v[114:117], v[134:137], v[174:177], v[114:117]
	v_mfma_f32_16x16x32_bf16 v[114:117], v[130:133], v[170:173], v[114:117]
	v_mfma_f32_16x16x32_bf16 v[102:105], v[130:133], v[178:181], v[102:105]
	v_mfma_f32_16x16x32_bf16 v[102:105], v[134:137], v[182:185], v[102:105]
	v_mfma_f32_16x16x32_bf16 v[94:97], v[142:145], v[182:185], v[94:97]
	v_mfma_f32_16x16x32_bf16 v[94:97], v[138:141], v[178:181], v[94:97]
	v_mfma_f32_16x16x32_bf16 v[78:81], v[138:141], v[186:189], v[78:81]
	v_mfma_f32_16x16x32_bf16 v[78:81], v[142:145], v[212:215], v[78:81]
	v_mfma_f32_16x16x32_bf16 v[86:89], v[134:137], v[212:215], v[86:89]
	v_mfma_f32_16x16x32_bf16 v[86:89], v[130:133], v[186:189], v[86:89]
	v_mfma_f32_16x16x32_bf16 v[118:121], v[146:149], v[162:165], v[118:121]
	v_mfma_f32_16x16x32_bf16 v[118:121], v[150:153], v[166:169], v[118:121]
	v_mfma_f32_16x16x32_bf16 v[110:113], v[158:161], v[166:169], v[110:113]
	v_mfma_f32_16x16x32_bf16 v[110:113], v[154:157], v[162:165], v[110:113]
	v_mfma_f32_16x16x32_bf16 v[90:93], v[154:157], v[170:173], v[90:93]
	v_mfma_f32_16x16x32_bf16 v[90:93], v[158:161], v[174:177], v[90:93]
	v_mfma_f32_16x16x32_bf16 v[98:101], v[150:153], v[174:177], v[98:101]
	v_mfma_f32_16x16x32_bf16 v[98:101], v[146:149], v[170:173], v[98:101]
	v_mfma_f32_16x16x32_bf16 v[82:85], v[146:149], v[178:181], v[82:85]
	v_mfma_f32_16x16x32_bf16 v[82:85], v[150:153], v[182:185], v[82:85]
	v_mfma_f32_16x16x32_bf16 v[74:77], v[158:161], v[182:185], v[74:77]
	v_mfma_f32_16x16x32_bf16 v[74:77], v[154:157], v[178:181], v[74:77]
	v_mfma_f32_16x16x32_bf16 v[66:69], v[154:157], v[186:189], v[66:69]
	v_mfma_f32_16x16x32_bf16 v[66:69], v[158:161], v[212:215], v[66:69]
	v_mfma_f32_16x16x32_bf16 v[70:73], v[150:153], v[212:215], v[70:73]
	v_mfma_f32_16x16x32_bf16 v[70:73], v[146:149], v[186:189], v[70:73]
	s_barrier
	s_mov_b32 m0, s79
	s_or_b32 s87, s86, 0x80
	ds_read_b128 v[162:165], v222 offset:49152
	ds_read_b128 v[166:169], v222 offset:50176
	ds_read_b128 v[170:173], v222 offset:51200
	ds_read_b128 v[174:177], v222 offset:52224
	ds_read_b128 v[178:181], v222 offset:53248
	ds_read_b128 v[182:185], v222 offset:54272
	ds_read_b128 v[186:189], v222 offset:55296
	ds_read_b128 v[212:215], v222 offset:56320
	buffer_load_dwordx4 v191, s[44:47], s87 offen lds
	s_mov_b32 m0, s80
	s_add_i32 s86, s86, 0x80080
	buffer_load_dwordx4 v217, s[44:47], s87 offen lds
	s_mov_b32 m0, s83
	s_nop 0
	buffer_load_dwordx4 v191, s[44:47], s86 offen lds
	s_mov_b32 m0, s92
	s_nop 0
	buffer_load_dwordx4 v217, s[44:47], s86 offen lds
	s_mov_b32 m0, s81
	s_nop 0
	buffer_load_dwordx4 v1, s[40:43], s85 offen lds
	s_mov_b32 m0, s82
	s_nop 0
	buffer_load_dwordx4 v216, s[40:43], s85 offen lds
	s_waitcnt vmcnt(8)
	s_waitcnt lgkmcnt(0)
	s_barrier
	v_mfma_f32_16x16x32_bf16 v[62:65], v[130:133], v[162:165], v[62:65]
	v_mfma_f32_16x16x32_bf16 v[62:65], v[134:137], v[166:169], v[62:65]
	v_mfma_f32_16x16x32_bf16 v[58:61], v[142:145], v[166:169], v[58:61]
	v_mfma_f32_16x16x32_bf16 v[58:61], v[138:141], v[162:165], v[58:61]
	v_mfma_f32_16x16x32_bf16 v[46:49], v[138:141], v[170:173], v[46:49]
	v_mfma_f32_16x16x32_bf16 v[46:49], v[142:145], v[174:177], v[46:49]
	v_mfma_f32_16x16x32_bf16 v[54:57], v[134:137], v[174:177], v[54:57]
	v_mfma_f32_16x16x32_bf16 v[54:57], v[130:133], v[170:173], v[54:57]
	v_mfma_f32_16x16x32_bf16 v[38:41], v[130:133], v[178:181], v[38:41]
	v_mfma_f32_16x16x32_bf16 v[38:41], v[134:137], v[182:185], v[38:41]
	v_mfma_f32_16x16x32_bf16 v[30:33], v[142:145], v[182:185], v[30:33]
	v_mfma_f32_16x16x32_bf16 v[30:33], v[138:141], v[178:181], v[30:33]
	v_mfma_f32_16x16x32_bf16 v[14:17], v[138:141], v[186:189], v[14:17]
	v_mfma_f32_16x16x32_bf16 v[14:17], v[142:145], v[212:215], v[14:17]
	v_mfma_f32_16x16x32_bf16 v[22:25], v[134:137], v[212:215], v[22:25]
	v_mfma_f32_16x16x32_bf16 v[22:25], v[130:133], v[186:189], v[22:25]
	v_mfma_f32_16x16x32_bf16 v[50:53], v[146:149], v[162:165], v[50:53]
	v_mfma_f32_16x16x32_bf16 v[50:53], v[150:153], v[166:169], v[50:53]
	v_mfma_f32_16x16x32_bf16 v[42:45], v[158:161], v[166:169], v[42:45]
	v_mfma_f32_16x16x32_bf16 v[42:45], v[154:157], v[162:165], v[42:45]
	v_mfma_f32_16x16x32_bf16 v[26:29], v[154:157], v[170:173], v[26:29]
	v_mfma_f32_16x16x32_bf16 v[26:29], v[158:161], v[174:177], v[26:29]
	v_mfma_f32_16x16x32_bf16 v[34:37], v[150:153], v[174:177], v[34:37]
	v_mfma_f32_16x16x32_bf16 v[34:37], v[146:149], v[170:173], v[34:37]
	v_mfma_f32_16x16x32_bf16 v[18:21], v[146:149], v[178:181], v[18:21]
	v_mfma_f32_16x16x32_bf16 v[18:21], v[150:153], v[182:185], v[18:21]
	v_mfma_f32_16x16x32_bf16 v[10:13], v[158:161], v[182:185], v[10:13]
	v_mfma_f32_16x16x32_bf16 v[10:13], v[154:157], v[178:181], v[10:13]
	v_mfma_f32_16x16x32_bf16 v[2:5], v[154:157], v[186:189], v[2:5]
	v_mfma_f32_16x16x32_bf16 v[2:5], v[158:161], v[212:215], v[2:5]
	v_mfma_f32_16x16x32_bf16 v[6:9], v[150:153], v[212:215], v[6:9]
	v_mfma_f32_16x16x32_bf16 v[6:9], v[146:149], v[186:189], v[6:9]
	s_barrier
	s_add_i32 s84, s84, 2
	s_addk_i32 s64, 0x100
	s_addk_i32 s65, 0x100
	s_cmp_gt_u32 s84, 29
	s_cbranch_scc0 .LBB0_114
	s_and_b64 vcc, exec, s[56:57]
	s_cbranch_vccz .LBB0_127
	s_barrier
	s_cmp_gt_i32 s61, 23
	s_mov_b64 s[46:47], -1
	s_cbranch_scc1 .LBB0_128

.LBB0_563:
	v_add_u32_e32 v3, 0x10000, v209
	ds_read_b128 v[140:143], v3
	ds_read_b128 v[144:147], v3 offset:1024
	ds_read_b128 v[148:151], v3 offset:2048
	ds_read_b128 v[152:155], v3 offset:3072
	v_add_u32_e32 v3, 0x14000, v209
	ds_read_b128 v[156:159], v3
	ds_read_b128 v[160:163], v3 offset:1024
	ds_read_b128 v[164:167], v3 offset:2048
	ds_read_b128 v[168:171], v3 offset:3072
	s_add_i32 s10, s57, 0xfff80080
	s_cmp_eq_u32 s59, 12
	s_cselect_b32 s62, s2, s10
	s_cselect_b32 s61, s3, s58
	s_add_i32 s60, s62, 0x80
	s_mov_b32 m0, s44
	ds_read_b128 v[172:175], v210
	ds_read_b128 v[176:179], v210 offset:1024
	ds_read_b128 v[180:183], v210 offset:2048
	ds_read_b128 v[184:187], v210 offset:3072
	ds_read_b128 v[188:191], v210 offset:4096
	ds_read_b128 v[192:195], v210 offset:5120
	ds_read_b128 v[196:199], v210 offset:6144
	ds_read_b128 v[200:203], v210 offset:7168
	buffer_load_dwordx4 v1, s[4:7], s57 offen lds
	s_mov_b32 m0, s45
	s_nop 0
	buffer_load_dwordx4 v206, s[4:7], s57 offen lds
	s_waitcnt vmcnt(8)
	s_waitcnt lgkmcnt(0)
	s_barrier
	v_mfma_f32_16x16x32_bf16 v[130:133], v[140:143], v[172:175], v[130:133]
	v_mfma_f32_16x16x32_bf16 v[130:133], v[144:147], v[176:179], v[130:133]
	v_mfma_f32_16x16x32_bf16 v[126:129], v[152:155], v[176:179], v[126:129]
	v_mfma_f32_16x16x32_bf16 v[126:129], v[148:151], v[172:175], v[126:129]
	v_mfma_f32_16x16x32_bf16 v[118:121], v[148:151], v[180:183], v[118:121]
	v_mfma_f32_16x16x32_bf16 v[118:121], v[152:155], v[184:187], v[118:121]
	v_mfma_f32_16x16x32_bf16 v[122:125], v[144:147], v[184:187], v[122:125]
	v_mfma_f32_16x16x32_bf16 v[122:125], v[140:143], v[180:183], v[122:125]
	v_mfma_f32_16x16x32_bf16 v[114:117], v[140:143], v[188:191], v[114:117]
	v_mfma_f32_16x16x32_bf16 v[114:117], v[144:147], v[192:195], v[114:117]
	v_mfma_f32_16x16x32_bf16 v[110:113], v[152:155], v[192:195], v[110:113]
	v_mfma_f32_16x16x32_bf16 v[110:113], v[148:151], v[188:191], v[110:113]
	v_mfma_f32_16x16x32_bf16 v[102:105], v[148:151], v[196:199], v[102:105]
	v_mfma_f32_16x16x32_bf16 v[102:105], v[152:155], v[200:203], v[102:105]
	v_mfma_f32_16x16x32_bf16 v[106:109], v[144:147], v[200:203], v[106:109]
	v_mfma_f32_16x16x32_bf16 v[106:109], v[140:143], v[196:199], v[106:109]
	v_mfma_f32_16x16x32_bf16 v[98:101], v[156:159], v[172:175], v[98:101]
	v_mfma_f32_16x16x32_bf16 v[98:101], v[160:163], v[176:179], v[98:101]
	v_mfma_f32_16x16x32_bf16 v[94:97], v[168:171], v[176:179], v[94:97]
	v_mfma_f32_16x16x32_bf16 v[94:97], v[164:167], v[172:175], v[94:97]
	v_mfma_f32_16x16x32_bf16 v[86:89], v[164:167], v[180:183], v[86:89]
	v_mfma_f32_16x16x32_bf16 v[86:89], v[168:171], v[184:187], v[86:89]
	v_mfma_f32_16x16x32_bf16 v[90:93], v[160:163], v[184:187], v[90:93]
	v_mfma_f32_16x16x32_bf16 v[90:93], v[156:159], v[180:183], v[90:93]
	v_mfma_f32_16x16x32_bf16 v[82:85], v[156:159], v[188:191], v[82:85]
	v_mfma_f32_16x16x32_bf16 v[82:85], v[160:163], v[192:195], v[82:85]
	v_mfma_f32_16x16x32_bf16 v[78:81], v[168:171], v[192:195], v[78:81]
	v_mfma_f32_16x16x32_bf16 v[78:81], v[164:167], v[188:191], v[78:81]
	v_mfma_f32_16x16x32_bf16 v[70:73], v[164:167], v[196:199], v[70:73]
	v_mfma_f32_16x16x32_bf16 v[70:73], v[168:171], v[200:203], v[70:73]
	v_mfma_f32_16x16x32_bf16 v[74:77], v[160:163], v[200:203], v[74:77]
	v_mfma_f32_16x16x32_bf16 v[74:77], v[156:159], v[196:199], v[74:77]
	s_barrier
	s_mov_b32 m0, s28
	s_mov_b32 s10, s6
	s_mov_b32 s11, s7
	ds_read_b128 v[172:175], v210 offset:16384
	ds_read_b128 v[176:179], v210 offset:17408
	ds_read_b128 v[180:183], v210 offset:18432
	ds_read_b128 v[184:187], v210 offset:19456
	ds_read_b128 v[188:191], v210 offset:20480
	ds_read_b128 v[192:195], v210 offset:21504
	ds_read_b128 v[196:199], v210 offset:22528
	ds_read_b128 v[200:203], v210 offset:23552
	buffer_load_dwordx4 v135, s[8:11], s61 offen lds
	s_mov_b32 m0, s29
	s_add_i32 s63, s61, 0x80000
	buffer_load_dwordx4 v207, s[8:11], s61 offen lds
	s_mov_b32 m0, s30
	s_nop 0
	buffer_load_dwordx4 v135, s[8:11], s63 offen lds
	s_mov_b32 m0, s31
	s_nop 0
	buffer_load_dwordx4 v207, s[8:11], s63 offen lds
	s_mov_b32 m0, s27
	s_nop 0
	buffer_load_dwordx4 v1, s[4:7], s62 offen lds
	s_mov_b32 m0, s33
	s_nop 0
	buffer_load_dwordx4 v206, s[4:7], s62 offen lds
	s_waitcnt vmcnt(8)
	s_waitcnt lgkmcnt(0)
	s_barrier
	v_mfma_f32_16x16x32_bf16 v[66:69], v[140:143], v[172:175], v[66:69]
	v_mfma_f32_16x16x32_bf16 v[66:69], v[144:147], v[176:179], v[66:69]
	v_mfma_f32_16x16x32_bf16 v[62:65], v[152:155], v[176:179], v[62:65]
	v_mfma_f32_16x16x32_bf16 v[62:65], v[148:151], v[172:175], v[62:65]
	v_mfma_f32_16x16x32_bf16 v[54:57], v[148:151], v[180:183], v[54:57]
	v_mfma_f32_16x16x32_bf16 v[54:57], v[152:155], v[184:187], v[54:57]
	v_mfma_f32_16x16x32_bf16 v[58:61], v[144:147], v[184:187], v[58:61]
	v_mfma_f32_16x16x32_bf16 v[58:61], v[140:143], v[180:183], v[58:61]
	v_mfma_f32_16x16x32_bf16 v[50:53], v[140:143], v[188:191], v[50:53]
	v_mfma_f32_16x16x32_bf16 v[50:53], v[144:147], v[192:195], v[50:53]
	v_mfma_f32_16x16x32_bf16 v[46:49], v[152:155], v[192:195], v[46:49]
	v_mfma_f32_16x16x32_bf16 v[46:49], v[148:151], v[188:191], v[46:49]
	v_mfma_f32_16x16x32_bf16 v[38:41], v[148:151], v[196:199], v[38:41]
	v_mfma_f32_16x16x32_bf16 v[38:41], v[152:155], v[200:203], v[38:41]
	v_mfma_f32_16x16x32_bf16 v[42:45], v[144:147], v[200:203], v[42:45]
	v_mfma_f32_16x16x32_bf16 v[42:45], v[140:143], v[196:199], v[42:45]
	v_mfma_f32_16x16x32_bf16 v[34:37], v[156:159], v[172:175], v[34:37]
	v_mfma_f32_16x16x32_bf16 v[34:37], v[160:163], v[176:179], v[34:37]
	v_mfma_f32_16x16x32_bf16 v[30:33], v[164:167], v[172:175], v[30:33]
	v_mfma_f32_16x16x32_bf16 v[30:33], v[168:171], v[176:179], v[30:33]
	v_mfma_f32_16x16x32_bf16 v[26:29], v[156:159], v[180:183], v[26:29]
	v_mfma_f32_16x16x32_bf16 v[26:29], v[160:163], v[184:187], v[26:29]
	v_mfma_f32_16x16x32_bf16 v[22:25], v[164:167], v[180:183], v[22:25]
	v_mfma_f32_16x16x32_bf16 v[22:25], v[168:171], v[184:187], v[22:25]
	v_mfma_f32_16x16x32_bf16 v[18:21], v[156:159], v[188:191], v[18:21]
	v_mfma_f32_16x16x32_bf16 v[18:21], v[160:163], v[192:195], v[18:21]
	v_mfma_f32_16x16x32_bf16 v[14:17], v[164:167], v[188:191], v[14:17]
	v_mfma_f32_16x16x32_bf16 v[14:17], v[168:171], v[192:195], v[14:17]
	v_mfma_f32_16x16x32_bf16 v[10:13], v[156:159], v[196:199], v[10:13]
	v_mfma_f32_16x16x32_bf16 v[10:13], v[160:163], v[200:203], v[10:13]
	v_mfma_f32_16x16x32_bf16 v[4:7], v[164:167], v[196:199], v[6:9]
	v_mfma_f32_16x16x32_bf16 v[4:7], v[168:171], v[200:203], v[4:7]
	s_barrier
	v_add_u32_e32 v3, 0x18000, v209
	ds_read_b128 v[140:143], v3
	ds_read_b128 v[144:147], v3 offset:1024
	ds_read_b128 v[148:151], v3 offset:2048
	ds_read_b128 v[152:155], v3 offset:3072
	v_add_u32_e32 v3, 0x1c000, v209
	ds_read_b128 v[156:159], v3
	ds_read_b128 v[160:163], v3 offset:1024
	ds_read_b128 v[164:167], v3 offset:2048
	ds_read_b128 v[168:171], v3 offset:3072
	s_add_i32 s62, s62, 0x80000
	s_mov_b32 m0, s34
	ds_read_b128 v[172:175], v210 offset:32768
	ds_read_b128 v[176:179], v210 offset:33792
	ds_read_b128 v[180:183], v210 offset:34816
	ds_read_b128 v[184:187], v210 offset:35840
	ds_read_b128 v[188:191], v210 offset:36864
	ds_read_b128 v[192:195], v210 offset:37888
	ds_read_b128 v[196:199], v210 offset:38912
	ds_read_b128 v[200:203], v210 offset:39936
	buffer_load_dwordx4 v1, s[4:7], s62 offen lds
	s_mov_b32 m0, s35
	s_nop 0
	buffer_load_dwordx4 v206, s[4:7], s62 offen lds
	s_waitcnt vmcnt(8)
	s_waitcnt lgkmcnt(0)
	s_barrier
	v_mfma_f32_16x16x32_bf16 v[130:133], v[140:143], v[172:175], v[130:133]
	v_mfma_f32_16x16x32_bf16 v[130:133], v[144:147], v[176:179], v[130:133]
	v_mfma_f32_16x16x32_bf16 v[126:129], v[152:155], v[176:179], v[126:129]
	v_mfma_f32_16x16x32_bf16 v[126:129], v[148:151], v[172:175], v[126:129]
	v_mfma_f32_16x16x32_bf16 v[118:121], v[148:151], v[180:183], v[118:121]
	v_mfma_f32_16x16x32_bf16 v[118:121], v[152:155], v[184:187], v[118:121]
	v_mfma_f32_16x16x32_bf16 v[122:125], v[144:147], v[184:187], v[122:125]
	v_mfma_f32_16x16x32_bf16 v[122:125], v[140:143], v[180:183], v[122:125]
	v_mfma_f32_16x16x32_bf16 v[114:117], v[140:143], v[188:191], v[114:117]
	v_mfma_f32_16x16x32_bf16 v[114:117], v[144:147], v[192:195], v[114:117]
	v_mfma_f32_16x16x32_bf16 v[110:113], v[152:155], v[192:195], v[110:113]
	v_mfma_f32_16x16x32_bf16 v[110:113], v[148:151], v[188:191], v[110:113]
	v_mfma_f32_16x16x32_bf16 v[102:105], v[148:151], v[196:199], v[102:105]
	v_mfma_f32_16x16x32_bf16 v[102:105], v[152:155], v[200:203], v[102:105]
	v_mfma_f32_16x16x32_bf16 v[106:109], v[144:147], v[200:203], v[106:109]
	v_mfma_f32_16x16x32_bf16 v[106:109], v[140:143], v[196:199], v[106:109]
	v_mfma_f32_16x16x32_bf16 v[98:101], v[156:159], v[172:175], v[98:101]
	v_mfma_f32_16x16x32_bf16 v[98:101], v[160:163], v[176:179], v[98:101]
	v_mfma_f32_16x16x32_bf16 v[94:97], v[168:171], v[176:179], v[94:97]
	v_mfma_f32_16x16x32_bf16 v[94:97], v[164:167], v[172:175], v[94:97]
	v_mfma_f32_16x16x32_bf16 v[86:89], v[164:167], v[180:183], v[86:89]
	v_mfma_f32_16x16x32_bf16 v[86:89], v[168:171], v[184:187], v[86:89]
	v_mfma_f32_16x16x32_bf16 v[90:93], v[160:163], v[184:187], v[90:93]
	v_mfma_f32_16x16x32_bf16 v[90:93], v[156:159], v[180:183], v[90:93]
	v_mfma_f32_16x16x32_bf16 v[82:85], v[156:159], v[188:191], v[82:85]
	v_mfma_f32_16x16x32_bf16 v[82:85], v[160:163], v[192:195], v[82:85]
	v_mfma_f32_16x16x32_bf16 v[78:81], v[168:171], v[192:195], v[78:81]
	v_mfma_f32_16x16x32_bf16 v[78:81], v[164:167], v[188:191], v[78:81]
	v_mfma_f32_16x16x32_bf16 v[70:73], v[164:167], v[196:199], v[70:73]
	v_mfma_f32_16x16x32_bf16 v[70:73], v[168:171], v[200:203], v[70:73]
	v_mfma_f32_16x16x32_bf16 v[74:77], v[160:163], v[200:203], v[74:77]
	v_mfma_f32_16x16x32_bf16 v[74:77], v[156:159], v[196:199], v[74:77]
	s_barrier
	s_mov_b32 m0, s38
	s_add_i32 s62, s61, 0x80
	ds_read_b128 v[172:175], v210 offset:49152
	ds_read_b128 v[176:179], v210 offset:50176
	ds_read_b128 v[180:183], v210 offset:51200
	ds_read_b128 v[184:187], v210 offset:52224
	ds_read_b128 v[188:191], v210 offset:53248
	ds_read_b128 v[192:195], v210 offset:54272
	ds_read_b128 v[196:199], v210 offset:55296
	ds_read_b128 v[200:203], v210 offset:56320
	buffer_load_dwordx4 v135, s[8:11], s62 offen lds
	s_mov_b32 m0, s39
	s_add_i32 s61, s61, 0x80080
	buffer_load_dwordx4 v207, s[8:11], s62 offen lds
	s_mov_b32 m0, s42
	s_nop 0
	buffer_load_dwordx4 v135, s[8:11], s61 offen lds
	s_mov_b32 m0, s43
	s_nop 0
	buffer_load_dwordx4 v207, s[8:11], s61 offen lds
	s_mov_b32 m0, s40
	s_nop 0
	buffer_load_dwordx4 v1, s[4:7], s60 offen lds
	s_mov_b32 m0, s41
	s_nop 0
	buffer_load_dwordx4 v206, s[4:7], s60 offen lds
	s_waitcnt vmcnt(8)
	s_waitcnt lgkmcnt(0)
	s_barrier
	v_mfma_f32_16x16x32_bf16 v[66:69], v[140:143], v[172:175], v[66:69]
	v_mfma_f32_16x16x32_bf16 v[66:69], v[144:147], v[176:179], v[66:69]
	v_mfma_f32_16x16x32_bf16 v[62:65], v[152:155], v[176:179], v[62:65]
	v_mfma_f32_16x16x32_bf16 v[62:65], v[148:151], v[172:175], v[62:65]
	v_mfma_f32_16x16x32_bf16 v[54:57], v[148:151], v[180:183], v[54:57]
	v_mfma_f32_16x16x32_bf16 v[54:57], v[152:155], v[184:187], v[54:57]
	v_mfma_f32_16x16x32_bf16 v[58:61], v[144:147], v[184:187], v[58:61]
	v_mfma_f32_16x16x32_bf16 v[58:61], v[140:143], v[180:183], v[58:61]
	v_mfma_f32_16x16x32_bf16 v[50:53], v[140:143], v[188:191], v[50:53]
	v_mfma_f32_16x16x32_bf16 v[50:53], v[144:147], v[192:195], v[50:53]
	v_mfma_f32_16x16x32_bf16 v[46:49], v[152:155], v[192:195], v[46:49]
	v_mfma_f32_16x16x32_bf16 v[46:49], v[148:151], v[188:191], v[46:49]
	v_mfma_f32_16x16x32_bf16 v[38:41], v[148:151], v[196:199], v[38:41]
	v_mfma_f32_16x16x32_bf16 v[38:41], v[152:155], v[200:203], v[38:41]
	v_mfma_f32_16x16x32_bf16 v[42:45], v[144:147], v[200:203], v[42:45]
	v_mfma_f32_16x16x32_bf16 v[42:45], v[140:143], v[196:199], v[42:45]
	v_mfma_f32_16x16x32_bf16 v[34:37], v[156:159], v[172:175], v[34:37]
	v_mfma_f32_16x16x32_bf16 v[34:37], v[160:163], v[176:179], v[34:37]
	v_mfma_f32_16x16x32_bf16 v[30:33], v[164:167], v[172:175], v[30:33]
	v_mfma_f32_16x16x32_bf16 v[30:33], v[168:171], v[176:179], v[30:33]
	v_mfma_f32_16x16x32_bf16 v[26:29], v[156:159], v[180:183], v[26:29]
	v_mfma_f32_16x16x32_bf16 v[26:29], v[160:163], v[184:187], v[26:29]
	v_mfma_f32_16x16x32_bf16 v[22:25], v[164:167], v[180:183], v[22:25]
	v_mfma_f32_16x16x32_bf16 v[22:25], v[168:171], v[184:187], v[22:25]
	v_mfma_f32_16x16x32_bf16 v[18:21], v[156:159], v[188:191], v[18:21]
	v_mfma_f32_16x16x32_bf16 v[18:21], v[160:163], v[192:195], v[18:21]
	v_mfma_f32_16x16x32_bf16 v[14:17], v[164:167], v[188:191], v[14:17]
	v_mfma_f32_16x16x32_bf16 v[14:17], v[168:171], v[192:195], v[14:17]
	v_mfma_f32_16x16x32_bf16 v[8:11], v[156:159], v[196:199], v[10:13]
	v_mfma_f32_16x16x32_bf16 v[10:13], v[160:163], v[200:203], v[8:11]
	v_mfma_f32_16x16x32_bf16 v[4:7], v[164:167], v[196:199], v[4:7]
	v_mfma_f32_16x16x32_bf16 v[6:9], v[168:171], v[200:203], v[4:7]
	s_barrier
	s_add_i32 s59, s59, 2
	s_addk_i32 s57, 0x100
	s_addk_i32 s58, 0x100
	s_cmp_gt_u32 s59, 13
	s_cbranch_scc0 .LBB0_563
	s_and_b64 vcc, exec, s[20:21]
	s_cbranch_vccz .LBB0_566
	s_barrier

.LBB0_686:
	v_add_u32_e32 v152, 0x10000, v138
	v_add_u32_e32 v168, 0x14000, v138
	ds_read_b128 v[140:143], v152
	ds_read_b128 v[144:147], v152 offset:1024
	ds_read_b128 v[148:151], v152 offset:2048
	ds_read_b128 v[152:155], v152 offset:3072
	ds_read_b128 v[156:159], v168
	ds_read_b128 v[160:163], v168 offset:1024
	ds_read_b128 v[164:167], v168 offset:2048
	ds_read_b128 v[168:171], v168 offset:3072
	s_add_i32 s10, s33, s52
	s_add_i32 s53, s27, s52
	s_add_i32 s11, s10, 0x1000
	s_addk_i32 s53, 0x1000
	s_cmp_eq_u32 s52, 0
	s_cselect_b32 s55, s49, s11
	s_cselect_b32 s54, s50, s53
	s_or_b32 s53, s55, 0x80
	s_add_i32 s10, s10, 0x80f80
	s_mov_b32 m0, s43
	ds_read_b128 v[172:175], v139
	ds_read_b128 v[176:179], v139 offset:1024
	ds_read_b128 v[180:183], v139 offset:2048
	ds_read_b128 v[184:187], v139 offset:3072
	ds_read_b128 v[188:191], v139 offset:4096
	ds_read_b128 v[192:195], v139 offset:5120
	ds_read_b128 v[196:199], v139 offset:6144
	ds_read_b128 v[200:203], v139 offset:7168
	buffer_load_dwordx4 v134, s[4:7], s10 offen lds
	s_mov_b32 m0, s44
	s_nop 0
	buffer_load_dwordx4 v136, s[4:7], s10 offen lds
	s_waitcnt vmcnt(8)
	s_waitcnt lgkmcnt(0)
	s_barrier
	v_mfma_f32_16x16x32_bf16 v[126:129], v[140:143], v[172:175], v[126:129]
	v_mfma_f32_16x16x32_bf16 v[126:129], v[144:147], v[176:179], v[126:129]
	v_mfma_f32_16x16x32_bf16 v[122:125], v[152:155], v[176:179], v[122:125]
	v_mfma_f32_16x16x32_bf16 v[122:125], v[148:151], v[172:175], v[122:125]
	v_mfma_f32_16x16x32_bf16 v[106:109], v[148:151], v[180:183], v[106:109]
	v_mfma_f32_16x16x32_bf16 v[106:109], v[152:155], v[184:187], v[106:109]
	v_mfma_f32_16x16x32_bf16 v[110:113], v[144:147], v[184:187], v[110:113]
	v_mfma_f32_16x16x32_bf16 v[110:113], v[140:143], v[180:183], v[110:113]
	v_mfma_f32_16x16x32_bf16 v[98:101], v[140:143], v[188:191], v[98:101]
	v_mfma_f32_16x16x32_bf16 v[98:101], v[144:147], v[192:195], v[98:101]
	v_mfma_f32_16x16x32_bf16 v[90:93], v[152:155], v[192:195], v[90:93]
	v_mfma_f32_16x16x32_bf16 v[90:93], v[148:151], v[188:191], v[90:93]
	v_mfma_f32_16x16x32_bf16 v[74:77], v[148:151], v[196:199], v[74:77]
	v_mfma_f32_16x16x32_bf16 v[74:77], v[152:155], v[200:203], v[74:77]
	v_mfma_f32_16x16x32_bf16 v[82:85], v[144:147], v[200:203], v[82:85]
	v_mfma_f32_16x16x32_bf16 v[82:85], v[140:143], v[196:199], v[82:85]
	v_mfma_f32_16x16x32_bf16 v[118:121], v[156:159], v[172:175], v[118:121]
	v_mfma_f32_16x16x32_bf16 v[118:121], v[160:163], v[176:179], v[118:121]
	v_mfma_f32_16x16x32_bf16 v[114:117], v[168:171], v[176:179], v[114:117]
	v_mfma_f32_16x16x32_bf16 v[114:117], v[164:167], v[172:175], v[114:117]
	v_mfma_f32_16x16x32_bf16 v[94:97], v[164:167], v[180:183], v[94:97]
	v_mfma_f32_16x16x32_bf16 v[94:97], v[168:171], v[184:187], v[94:97]
	v_mfma_f32_16x16x32_bf16 v[102:105], v[160:163], v[184:187], v[102:105]
	v_mfma_f32_16x16x32_bf16 v[102:105], v[156:159], v[180:183], v[102:105]
	v_mfma_f32_16x16x32_bf16 v[86:89], v[156:159], v[188:191], v[86:89]
	v_mfma_f32_16x16x32_bf16 v[86:89], v[160:163], v[192:195], v[86:89]
	v_mfma_f32_16x16x32_bf16 v[78:81], v[168:171], v[192:195], v[78:81]
	v_mfma_f32_16x16x32_bf16 v[78:81], v[164:167], v[188:191], v[78:81]
	v_mfma_f32_16x16x32_bf16 v[66:69], v[164:167], v[196:199], v[66:69]
	v_mfma_f32_16x16x32_bf16 v[66:69], v[168:171], v[200:203], v[66:69]
	v_mfma_f32_16x16x32_bf16 v[70:73], v[160:163], v[200:203], v[70:73]
	v_mfma_f32_16x16x32_bf16 v[70:73], v[156:159], v[196:199], v[70:73]
	s_barrier
	s_mov_b32 m0, s26
	s_mov_b32 s10, s6
	s_mov_b32 s11, s7
	ds_read_b128 v[172:175], v139 offset:16384
	ds_read_b128 v[176:179], v139 offset:17408
	ds_read_b128 v[180:183], v139 offset:18432
	ds_read_b128 v[184:187], v139 offset:19456
	ds_read_b128 v[188:191], v139 offset:20480
	ds_read_b128 v[192:195], v139 offset:21504
	ds_read_b128 v[196:199], v139 offset:22528
	ds_read_b128 v[200:203], v139 offset:23552
	buffer_load_dwordx4 v135, s[8:11], s54 offen lds
	s_mov_b32 m0, s28
	s_add_i32 s56, s54, 0x80000
	buffer_load_dwordx4 v137, s[8:11], s54 offen lds
	s_mov_b32 m0, s29
	s_nop 0
	buffer_load_dwordx4 v135, s[8:11], s56 offen lds
	s_mov_b32 m0, s30
	s_nop 0
	buffer_load_dwordx4 v137, s[8:11], s56 offen lds
	s_mov_b32 m0, s25
	s_nop 0
	buffer_load_dwordx4 v134, s[4:7], s55 offen lds
	s_mov_b32 m0, s31
	s_nop 0
	buffer_load_dwordx4 v136, s[4:7], s55 offen lds
	s_waitcnt vmcnt(8)
	s_waitcnt lgkmcnt(0)
	s_barrier
	v_mfma_f32_16x16x32_bf16 v[62:65], v[140:143], v[172:175], v[62:65]
	v_mfma_f32_16x16x32_bf16 v[62:65], v[144:147], v[176:179], v[62:65]
	v_mfma_f32_16x16x32_bf16 v[58:61], v[152:155], v[176:179], v[58:61]
	v_mfma_f32_16x16x32_bf16 v[58:61], v[148:151], v[172:175], v[58:61]
	v_mfma_f32_16x16x32_bf16 v[42:45], v[148:151], v[180:183], v[42:45]
	v_mfma_f32_16x16x32_bf16 v[42:45], v[152:155], v[184:187], v[42:45]
	v_mfma_f32_16x16x32_bf16 v[46:49], v[144:147], v[184:187], v[46:49]
	v_mfma_f32_16x16x32_bf16 v[46:49], v[140:143], v[180:183], v[46:49]
	v_mfma_f32_16x16x32_bf16 v[30:33], v[140:143], v[188:191], v[30:33]
	v_mfma_f32_16x16x32_bf16 v[30:33], v[144:147], v[192:195], v[30:33]
	v_mfma_f32_16x16x32_bf16 v[26:29], v[152:155], v[192:195], v[26:29]
	v_mfma_f32_16x16x32_bf16 v[26:29], v[148:151], v[188:191], v[26:29]
	v_mfma_f32_16x16x32_bf16 v[10:13], v[148:151], v[196:199], v[10:13]
	v_mfma_f32_16x16x32_bf16 v[10:13], v[152:155], v[200:203], v[10:13]
	v_mfma_f32_16x16x32_bf16 v[14:17], v[144:147], v[200:203], v[14:17]
	v_mfma_f32_16x16x32_bf16 v[14:17], v[140:143], v[196:199], v[14:17]
	v_mfma_f32_16x16x32_bf16 v[54:57], v[156:159], v[172:175], v[54:57]
	v_mfma_f32_16x16x32_bf16 v[54:57], v[160:163], v[176:179], v[54:57]
	v_mfma_f32_16x16x32_bf16 v[50:53], v[168:171], v[176:179], v[50:53]
	v_mfma_f32_16x16x32_bf16 v[50:53], v[164:167], v[172:175], v[50:53]
	v_mfma_f32_16x16x32_bf16 v[34:37], v[164:167], v[180:183], v[34:37]
	v_mfma_f32_16x16x32_bf16 v[34:37], v[168:171], v[184:187], v[34:37]
	v_mfma_f32_16x16x32_bf16 v[38:41], v[160:163], v[184:187], v[38:41]
	v_mfma_f32_16x16x32_bf16 v[38:41], v[156:159], v[180:183], v[38:41]
	v_mfma_f32_16x16x32_bf16 v[22:25], v[156:159], v[188:191], v[22:25]
	v_mfma_f32_16x16x32_bf16 v[22:25], v[160:163], v[192:195], v[22:25]
	v_mfma_f32_16x16x32_bf16 v[18:21], v[168:171], v[192:195], v[18:21]
	v_mfma_f32_16x16x32_bf16 v[18:21], v[164:167], v[188:191], v[18:21]
	v_mfma_f32_16x16x32_bf16 v[2:5], v[164:167], v[196:199], v[2:5]
	v_mfma_f32_16x16x32_bf16 v[2:5], v[168:171], v[200:203], v[2:5]
	v_mfma_f32_16x16x32_bf16 v[6:9], v[160:163], v[200:203], v[6:9]
	v_mfma_f32_16x16x32_bf16 v[6:9], v[156:159], v[196:199], v[6:9]
	s_barrier
	v_add_u32_e32 v152, 0x18000, v138
	v_add_u32_e32 v168, 0x1c000, v138
	ds_read_b128 v[140:143], v152
	ds_read_b128 v[144:147], v152 offset:1024
	ds_read_b128 v[148:151], v152 offset:2048
	ds_read_b128 v[152:155], v152 offset:3072
	ds_read_b128 v[156:159], v168
	ds_read_b128 v[160:163], v168 offset:1024
	ds_read_b128 v[164:167], v168 offset:2048
	ds_read_b128 v[168:171], v168 offset:3072
	s_add_i32 s55, s55, 0x80000
	s_mov_b32 m0, s34
	ds_read_b128 v[172:175], v139 offset:32768
	ds_read_b128 v[176:179], v139 offset:33792
	ds_read_b128 v[180:183], v139 offset:34816
	ds_read_b128 v[184:187], v139 offset:35840
	ds_read_b128 v[188:191], v139 offset:36864
	ds_read_b128 v[192:195], v139 offset:37888
	ds_read_b128 v[196:199], v139 offset:38912
	ds_read_b128 v[200:203], v139 offset:39936
	buffer_load_dwordx4 v134, s[4:7], s55 offen lds
	s_mov_b32 m0, s35
	s_nop 0
	buffer_load_dwordx4 v136, s[4:7], s55 offen lds
	s_waitcnt vmcnt(8)
	s_waitcnt lgkmcnt(0)
	s_barrier
	v_mfma_f32_16x16x32_bf16 v[126:129], v[140:143], v[172:175], v[126:129]
	v_mfma_f32_16x16x32_bf16 v[126:129], v[144:147], v[176:179], v[126:129]
	v_mfma_f32_16x16x32_bf16 v[122:125], v[152:155], v[176:179], v[122:125]
	v_mfma_f32_16x16x32_bf16 v[122:125], v[148:151], v[172:175], v[122:125]
	v_mfma_f32_16x16x32_bf16 v[106:109], v[148:151], v[180:183], v[106:109]
	v_mfma_f32_16x16x32_bf16 v[106:109], v[152:155], v[184:187], v[106:109]
	v_mfma_f32_16x16x32_bf16 v[110:113], v[144:147], v[184:187], v[110:113]
	v_mfma_f32_16x16x32_bf16 v[110:113], v[140:143], v[180:183], v[110:113]
	v_mfma_f32_16x16x32_bf16 v[98:101], v[140:143], v[188:191], v[98:101]
	v_mfma_f32_16x16x32_bf16 v[98:101], v[144:147], v[192:195], v[98:101]
	v_mfma_f32_16x16x32_bf16 v[90:93], v[152:155], v[192:195], v[90:93]
	v_mfma_f32_16x16x32_bf16 v[90:93], v[148:151], v[188:191], v[90:93]
	v_mfma_f32_16x16x32_bf16 v[74:77], v[148:151], v[196:199], v[74:77]
	v_mfma_f32_16x16x32_bf16 v[74:77], v[152:155], v[200:203], v[74:77]
	v_mfma_f32_16x16x32_bf16 v[82:85], v[144:147], v[200:203], v[82:85]
	v_mfma_f32_16x16x32_bf16 v[82:85], v[140:143], v[196:199], v[82:85]
	v_mfma_f32_16x16x32_bf16 v[118:121], v[156:159], v[172:175], v[118:121]
	v_mfma_f32_16x16x32_bf16 v[118:121], v[160:163], v[176:179], v[118:121]
	v_mfma_f32_16x16x32_bf16 v[114:117], v[168:171], v[176:179], v[114:117]
	v_mfma_f32_16x16x32_bf16 v[114:117], v[164:167], v[172:175], v[114:117]
	v_mfma_f32_16x16x32_bf16 v[94:97], v[164:167], v[180:183], v[94:97]
	v_mfma_f32_16x16x32_bf16 v[94:97], v[168:171], v[184:187], v[94:97]
	v_mfma_f32_16x16x32_bf16 v[102:105], v[160:163], v[184:187], v[102:105]
	v_mfma_f32_16x16x32_bf16 v[102:105], v[156:159], v[180:183], v[102:105]
	v_mfma_f32_16x16x32_bf16 v[86:89], v[156:159], v[188:191], v[86:89]
	v_mfma_f32_16x16x32_bf16 v[86:89], v[160:163], v[192:195], v[86:89]
	v_mfma_f32_16x16x32_bf16 v[78:81], v[168:171], v[192:195], v[78:81]
	v_mfma_f32_16x16x32_bf16 v[78:81], v[164:167], v[188:191], v[78:81]
	v_mfma_f32_16x16x32_bf16 v[66:69], v[164:167], v[196:199], v[66:69]
	v_mfma_f32_16x16x32_bf16 v[66:69], v[168:171], v[200:203], v[66:69]
	v_mfma_f32_16x16x32_bf16 v[70:73], v[160:163], v[200:203], v[70:73]
	v_mfma_f32_16x16x32_bf16 v[70:73], v[156:159], v[196:199], v[70:73]
	s_barrier
	s_mov_b32 m0, s36
	s_or_b32 s55, s54, 0x80
	ds_read_b128 v[172:175], v139 offset:49152
	ds_read_b128 v[176:179], v139 offset:50176
	ds_read_b128 v[180:183], v139 offset:51200
	ds_read_b128 v[184:187], v139 offset:52224
	ds_read_b128 v[188:191], v139 offset:53248
	ds_read_b128 v[192:195], v139 offset:54272
	ds_read_b128 v[196:199], v139 offset:55296
	ds_read_b128 v[200:203], v139 offset:56320
	buffer_load_dwordx4 v135, s[8:11], s55 offen lds
	s_mov_b32 m0, s37
	s_add_i32 s54, s54, 0x80080
	buffer_load_dwordx4 v137, s[8:11], s55 offen lds
	s_mov_b32 m0, s41
	s_nop 0
	buffer_load_dwordx4 v135, s[8:11], s54 offen lds
	s_mov_b32 m0, s42
	s_nop 0
	buffer_load_dwordx4 v137, s[8:11], s54 offen lds
	s_mov_b32 m0, s38
	s_nop 0
	buffer_load_dwordx4 v134, s[4:7], s53 offen lds
	s_mov_b32 m0, s40
	s_nop 0
	buffer_load_dwordx4 v136, s[4:7], s53 offen lds
	s_waitcnt vmcnt(8)
	s_waitcnt lgkmcnt(0)
	s_barrier
	v_mfma_f32_16x16x32_bf16 v[62:65], v[140:143], v[172:175], v[62:65]
	v_mfma_f32_16x16x32_bf16 v[62:65], v[144:147], v[176:179], v[62:65]
	v_mfma_f32_16x16x32_bf16 v[58:61], v[152:155], v[176:179], v[58:61]
	v_mfma_f32_16x16x32_bf16 v[58:61], v[148:151], v[172:175], v[58:61]
	v_mfma_f32_16x16x32_bf16 v[42:45], v[148:151], v[180:183], v[42:45]
	v_mfma_f32_16x16x32_bf16 v[42:45], v[152:155], v[184:187], v[42:45]
	v_mfma_f32_16x16x32_bf16 v[46:49], v[144:147], v[184:187], v[46:49]
	v_mfma_f32_16x16x32_bf16 v[46:49], v[140:143], v[180:183], v[46:49]
	v_mfma_f32_16x16x32_bf16 v[30:33], v[140:143], v[188:191], v[30:33]
	v_mfma_f32_16x16x32_bf16 v[30:33], v[144:147], v[192:195], v[30:33]
	v_mfma_f32_16x16x32_bf16 v[26:29], v[152:155], v[192:195], v[26:29]
	v_mfma_f32_16x16x32_bf16 v[26:29], v[148:151], v[188:191], v[26:29]
	v_mfma_f32_16x16x32_bf16 v[10:13], v[148:151], v[196:199], v[10:13]
	v_mfma_f32_16x16x32_bf16 v[10:13], v[152:155], v[200:203], v[10:13]
	v_mfma_f32_16x16x32_bf16 v[14:17], v[144:147], v[200:203], v[14:17]
	v_mfma_f32_16x16x32_bf16 v[14:17], v[140:143], v[196:199], v[14:17]
	v_mfma_f32_16x16x32_bf16 v[54:57], v[156:159], v[172:175], v[54:57]
	v_mfma_f32_16x16x32_bf16 v[54:57], v[160:163], v[176:179], v[54:57]
	v_mfma_f32_16x16x32_bf16 v[50:53], v[168:171], v[176:179], v[50:53]
	v_mfma_f32_16x16x32_bf16 v[50:53], v[164:167], v[172:175], v[50:53]
	v_mfma_f32_16x16x32_bf16 v[34:37], v[164:167], v[180:183], v[34:37]
	v_mfma_f32_16x16x32_bf16 v[34:37], v[168:171], v[184:187], v[34:37]
	v_mfma_f32_16x16x32_bf16 v[38:41], v[160:163], v[184:187], v[38:41]
	v_mfma_f32_16x16x32_bf16 v[38:41], v[156:159], v[180:183], v[38:41]
	v_mfma_f32_16x16x32_bf16 v[22:25], v[156:159], v[188:191], v[22:25]
	v_mfma_f32_16x16x32_bf16 v[22:25], v[160:163], v[192:195], v[22:25]
	v_mfma_f32_16x16x32_bf16 v[18:21], v[168:171], v[192:195], v[18:21]
	v_mfma_f32_16x16x32_bf16 v[18:21], v[164:167], v[188:191], v[18:21]
	v_mfma_f32_16x16x32_bf16 v[2:5], v[164:167], v[196:199], v[2:5]
	v_mfma_f32_16x16x32_bf16 v[2:5], v[168:171], v[200:203], v[2:5]
	v_mfma_f32_16x16x32_bf16 v[6:9], v[160:163], v[200:203], v[6:9]
	v_mfma_f32_16x16x32_bf16 v[6:9], v[156:159], v[196:199], v[6:9]
	s_barrier
	s_add_i32 s51, s51, 2
	s_addk_i32 s52, 0x100
	s_cmp_gt_u32 s51, 29
	s_cbranch_scc0 .LBB0_686
	s_andn2_b64 vcc, exec, s[2:3]
	s_cbranch_vccnz .LBB0_678
	v_mov_b32_e32 v2, 0
	s_mov_b32 s14, s46
	s_mov_b32 s15, s47
	s_mov_b32 s27, s48
	s_mov_b32 s33, s13
	s_mov_b32 s45, s12
	v_mov_b32_e32 v3, v2
	v_mov_b32_e32 v4, v2
	v_mov_b32_e32 v5, v2
	v_mov_b32_e32 v6, v2
	v_mov_b32_e32 v7, v2
	v_mov_b32_e32 v8, v2
	v_mov_b32_e32 v9, v2
	v_mov_b32_e32 v18, v2
	v_mov_b32_e32 v19, v2
	v_mov_b32_e32 v20, v2
	v_mov_b32_e32 v21, v2
	v_mov_b32_e32 v22, v2
	v_mov_b32_e32 v23, v2
	v_mov_b32_e32 v24, v2
	v_mov_b32_e32 v25, v2
	v_mov_b32_e32 v34, v2
	v_mov_b32_e32 v35, v2
	v_mov_b32_e32 v36, v2
	v_mov_b32_e32 v37, v2
	v_mov_b32_e32 v38, v2
	v_mov_b32_e32 v39, v2
	v_mov_b32_e32 v40, v2
	v_mov_b32_e32 v41, v2
	v_mov_b32_e32 v50, v2
	v_mov_b32_e32 v51, v2
	v_mov_b32_e32 v52, v2
	v_mov_b32_e32 v53, v2
	v_mov_b32_e32 v54, v2
	v_mov_b32_e32 v55, v2
	v_mov_b32_e32 v56, v2
	v_mov_b32_e32 v57, v2
	v_mov_b32_e32 v10, v2
	v_mov_b32_e32 v11, v2
	v_mov_b32_e32 v12, v2
	v_mov_b32_e32 v13, v2
	v_mov_b32_e32 v14, v2
	v_mov_b32_e32 v15, v2
	v_mov_b32_e32 v16, v2
	v_mov_b32_e32 v17, v2
	v_mov_b32_e32 v26, v2
	v_mov_b32_e32 v27, v2
	v_mov_b32_e32 v28, v2
	v_mov_b32_e32 v29, v2
	v_mov_b32_e32 v30, v2
	v_mov_b32_e32 v31, v2
	v_mov_b32_e32 v32, v2
	v_mov_b32_e32 v33, v2
	v_mov_b32_e32 v42, v2
	v_mov_b32_e32 v43, v2
	v_mov_b32_e32 v44, v2
	v_mov_b32_e32 v45, v2
	v_mov_b32_e32 v46, v2
	v_mov_b32_e32 v47, v2
	v_mov_b32_e32 v48, v2
	v_mov_b32_e32 v49, v2
	v_mov_b32_e32 v58, v2
	v_mov_b32_e32 v59, v2
	v_mov_b32_e32 v60, v2
	v_mov_b32_e32 v61, v2
	v_mov_b32_e32 v62, v2
	v_mov_b32_e32 v63, v2
	v_mov_b32_e32 v64, v2
	v_mov_b32_e32 v65, v2
	v_mov_b32_e32 v66, v2
	v_mov_b32_e32 v67, v2
	v_mov_b32_e32 v68, v2
	v_mov_b32_e32 v69, v2
	v_mov_b32_e32 v70, v2
	v_mov_b32_e32 v71, v2
	v_mov_b32_e32 v72, v2
	v_mov_b32_e32 v73, v2
	v_mov_b32_e32 v78, v2
	v_mov_b32_e32 v79, v2
	v_mov_b32_e32 v80, v2
	v_mov_b32_e32 v81, v2
	v_mov_b32_e32 v86, v2
	v_mov_b32_e32 v87, v2
	v_mov_b32_e32 v88, v2
	v_mov_b32_e32 v89, v2
	v_mov_b32_e32 v94, v2
	v_mov_b32_e32 v95, v2
	v_mov_b32_e32 v96, v2
	v_mov_b32_e32 v97, v2
	v_mov_b32_e32 v102, v2
	v_mov_b32_e32 v103, v2
	v_mov_b32_e32 v104, v2
	v_mov_b32_e32 v105, v2
	v_mov_b32_e32 v114, v2
	v_mov_b32_e32 v115, v2
	v_mov_b32_e32 v116, v2
	v_mov_b32_e32 v117, v2
	v_mov_b32_e32 v118, v2
	v_mov_b32_e32 v119, v2
	v_mov_b32_e32 v120, v2
	v_mov_b32_e32 v121, v2
	v_mov_b32_e32 v74, v2
	v_mov_b32_e32 v75, v2
	v_mov_b32_e32 v76, v2
	v_mov_b32_e32 v77, v2
	v_mov_b32_e32 v82, v2
	v_mov_b32_e32 v83, v2
	v_mov_b32_e32 v84, v2
	v_mov_b32_e32 v85, v2
	v_mov_b32_e32 v90, v2
	v_mov_b32_e32 v91, v2
	v_mov_b32_e32 v92, v2
	v_mov_b32_e32 v93, v2
	v_mov_b32_e32 v98, v2
	v_mov_b32_e32 v99, v2
	v_mov_b32_e32 v100, v2
	v_mov_b32_e32 v101, v2
	v_mov_b32_e32 v106, v2
	v_mov_b32_e32 v107, v2
	v_mov_b32_e32 v108, v2
	v_mov_b32_e32 v109, v2
	v_mov_b32_e32 v110, v2
	v_mov_b32_e32 v111, v2
	v_mov_b32_e32 v112, v2
	v_mov_b32_e32 v113, v2
	v_mov_b32_e32 v122, v2
	v_mov_b32_e32 v123, v2
	v_mov_b32_e32 v124, v2
	v_mov_b32_e32 v125, v2
	v_mov_b32_e32 v126, v2
	v_mov_b32_e32 v127, v2
	v_mov_b32_e32 v128, v2
	v_mov_b32_e32 v129, v2
	s_branch .LBB0_678

.LBB0_907:
	v_add_u32_e32 v166, 0x10000, v179
	ds_read_b128 v[162:165], v166
	ds_read_b128 v[182:185], v166 offset:1024
	ds_read_b128 v[186:189], v166 offset:2048
	ds_read_b128 v[190:193], v166 offset:3072
	v_add_u32_e32 v166, 0x14000, v179
	ds_read_b128 v[194:197], v166
	ds_read_b128 v[198:201], v166 offset:1024
	ds_read_b128 v[202:205], v166 offset:2048
	ds_read_b128 v[206:209], v166 offset:3072
	s_add_i32 s10, s45, s64
	s_add_i32 s26, s40, s64
	s_add_i32 s11, s10, 0x1000
	s_addk_i32 s26, 0x1000
	s_cmp_eq_u32 s64, 0
	s_cselect_b32 s29, s62, s11
	s_cselect_b32 s27, s63, s26
	s_add_i32 s26, s29, 0x80
	s_add_i32 s28, s27, 0x80
	s_add_i32 s10, s10, 0x80f80
	s_mov_b32 m0, s55
	ds_read_b128 v[210:213], v180
	ds_read_b128 v[214:217], v180 offset:1024
	ds_read_b128 v[218:221], v180 offset:2048
	ds_read_b128 v[222:225], v180 offset:3072
	ds_read_b128 v[226:229], v180 offset:4096
	ds_read_b128 v[230:233], v180 offset:5120
	ds_read_b128 v[234:237], v180 offset:6144
	ds_read_b128 v[238:241], v180 offset:7168
	buffer_load_dwordx4 v1, s[4:7], s10 offen lds
	s_mov_b32 m0, s56
	s_nop 0
	buffer_load_dwordx4 v175, s[4:7], s10 offen lds
	s_waitcnt vmcnt(8)
	s_waitcnt lgkmcnt(0)
	s_barrier
	v_mfma_f32_16x16x32_bf16 v[126:129], v[162:165], v[210:213], v[126:129]
	v_mfma_f32_16x16x32_bf16 v[126:129], v[182:185], v[214:217], v[126:129]
	v_mfma_f32_16x16x32_bf16 v[122:125], v[190:193], v[214:217], v[122:125]
	v_mfma_f32_16x16x32_bf16 v[122:125], v[186:189], v[210:213], v[122:125]
	v_mfma_f32_16x16x32_bf16 v[114:117], v[186:189], v[218:221], v[114:117]
	v_mfma_f32_16x16x32_bf16 v[114:117], v[190:193], v[222:225], v[114:117]
	v_mfma_f32_16x16x32_bf16 v[118:121], v[182:185], v[222:225], v[118:121]
	v_mfma_f32_16x16x32_bf16 v[118:121], v[162:165], v[218:221], v[118:121]
	v_mfma_f32_16x16x32_bf16 v[110:113], v[162:165], v[226:229], v[110:113]
	v_mfma_f32_16x16x32_bf16 v[110:113], v[182:185], v[230:233], v[110:113]
	v_mfma_f32_16x16x32_bf16 v[106:109], v[190:193], v[230:233], v[106:109]
	v_mfma_f32_16x16x32_bf16 v[106:109], v[186:189], v[226:229], v[106:109]
	v_mfma_f32_16x16x32_bf16 v[98:101], v[186:189], v[234:237], v[98:101]
	v_mfma_f32_16x16x32_bf16 v[98:101], v[190:193], v[238:241], v[98:101]
	v_mfma_f32_16x16x32_bf16 v[102:105], v[182:185], v[238:241], v[102:105]
	v_mfma_f32_16x16x32_bf16 v[102:105], v[162:165], v[234:237], v[102:105]
	v_mfma_f32_16x16x32_bf16 v[94:97], v[194:197], v[210:213], v[94:97]
	v_mfma_f32_16x16x32_bf16 v[94:97], v[198:201], v[214:217], v[94:97]
	v_mfma_f32_16x16x32_bf16 v[90:93], v[206:209], v[214:217], v[90:93]
	v_mfma_f32_16x16x32_bf16 v[90:93], v[202:205], v[210:213], v[90:93]
	v_mfma_f32_16x16x32_bf16 v[82:85], v[202:205], v[218:221], v[82:85]
	v_mfma_f32_16x16x32_bf16 v[82:85], v[206:209], v[222:225], v[82:85]
	v_mfma_f32_16x16x32_bf16 v[86:89], v[198:201], v[222:225], v[86:89]
	v_mfma_f32_16x16x32_bf16 v[86:89], v[194:197], v[218:221], v[86:89]
	v_mfma_f32_16x16x32_bf16 v[78:81], v[194:197], v[226:229], v[78:81]
	v_mfma_f32_16x16x32_bf16 v[78:81], v[198:201], v[230:233], v[78:81]
	v_mfma_f32_16x16x32_bf16 v[74:77], v[206:209], v[230:233], v[74:77]
	v_mfma_f32_16x16x32_bf16 v[74:77], v[202:205], v[226:229], v[74:77]
	v_mfma_f32_16x16x32_bf16 v[66:69], v[202:205], v[234:237], v[66:69]
	v_mfma_f32_16x16x32_bf16 v[66:69], v[206:209], v[238:241], v[66:69]
	v_mfma_f32_16x16x32_bf16 v[70:73], v[198:201], v[238:241], v[70:73]
	v_mfma_f32_16x16x32_bf16 v[70:73], v[194:197], v[234:237], v[70:73]
	s_barrier
	s_mov_b32 m0, s37
	s_mov_b32 s10, s6
	s_mov_b32 s11, s7
	ds_read_b128 v[210:213], v180 offset:16384
	ds_read_b128 v[214:217], v180 offset:17408
	ds_read_b128 v[218:221], v180 offset:18432
	ds_read_b128 v[222:225], v180 offset:19456
	ds_read_b128 v[226:229], v180 offset:20480
	ds_read_b128 v[230:233], v180 offset:21504
	ds_read_b128 v[234:237], v180 offset:22528
	ds_read_b128 v[238:241], v180 offset:23552
	buffer_load_dwordx4 v174, s[8:11], s27 offen lds
	s_mov_b32 m0, s38
	s_add_i32 s66, s27, 0x80000
	buffer_load_dwordx4 v176, s[8:11], s27 offen lds
	s_mov_b32 m0, s39
	s_nop 0
	buffer_load_dwordx4 v174, s[8:11], s66 offen lds
	s_mov_b32 m0, s41
	s_nop 0
	buffer_load_dwordx4 v176, s[8:11], s66 offen lds
	s_mov_b32 m0, s36
	s_nop 0
	buffer_load_dwordx4 v1, s[4:7], s29 offen lds
	s_mov_b32 m0, s42
	s_nop 0
	buffer_load_dwordx4 v175, s[4:7], s29 offen lds
	s_waitcnt vmcnt(8)
	s_waitcnt lgkmcnt(0)
	s_barrier
	v_mfma_f32_16x16x32_bf16 v[62:65], v[162:165], v[210:213], v[62:65]
	v_mfma_f32_16x16x32_bf16 v[62:65], v[182:185], v[214:217], v[62:65]
	v_mfma_f32_16x16x32_bf16 v[58:61], v[190:193], v[214:217], v[58:61]
	v_mfma_f32_16x16x32_bf16 v[58:61], v[186:189], v[210:213], v[58:61]
	v_mfma_f32_16x16x32_bf16 v[50:53], v[186:189], v[218:221], v[50:53]
	v_mfma_f32_16x16x32_bf16 v[50:53], v[190:193], v[222:225], v[50:53]
	v_mfma_f32_16x16x32_bf16 v[54:57], v[182:185], v[222:225], v[54:57]
	v_mfma_f32_16x16x32_bf16 v[54:57], v[162:165], v[218:221], v[54:57]
	v_mfma_f32_16x16x32_bf16 v[46:49], v[162:165], v[226:229], v[46:49]
	v_mfma_f32_16x16x32_bf16 v[46:49], v[182:185], v[230:233], v[46:49]
	v_mfma_f32_16x16x32_bf16 v[42:45], v[190:193], v[230:233], v[42:45]
	v_mfma_f32_16x16x32_bf16 v[42:45], v[186:189], v[226:229], v[42:45]
	v_mfma_f32_16x16x32_bf16 v[34:37], v[186:189], v[234:237], v[34:37]
	v_mfma_f32_16x16x32_bf16 v[34:37], v[190:193], v[238:241], v[34:37]
	v_mfma_f32_16x16x32_bf16 v[38:41], v[182:185], v[238:241], v[38:41]
	v_mfma_f32_16x16x32_bf16 v[38:41], v[162:165], v[234:237], v[38:41]
	v_mfma_f32_16x16x32_bf16 v[30:33], v[194:197], v[210:213], v[30:33]
	v_mfma_f32_16x16x32_bf16 v[30:33], v[198:201], v[214:217], v[30:33]
	v_mfma_f32_16x16x32_bf16 v[26:29], v[206:209], v[214:217], v[26:29]
	v_mfma_f32_16x16x32_bf16 v[26:29], v[202:205], v[210:213], v[26:29]
	v_mfma_f32_16x16x32_bf16 v[18:21], v[202:205], v[218:221], v[18:21]
	v_mfma_f32_16x16x32_bf16 v[18:21], v[206:209], v[222:225], v[18:21]
	v_mfma_f32_16x16x32_bf16 v[22:25], v[198:201], v[222:225], v[22:25]
	v_mfma_f32_16x16x32_bf16 v[22:25], v[194:197], v[218:221], v[22:25]
	v_mfma_f32_16x16x32_bf16 v[14:17], v[194:197], v[226:229], v[14:17]
	v_mfma_f32_16x16x32_bf16 v[14:17], v[198:201], v[230:233], v[14:17]
	v_mfma_f32_16x16x32_bf16 v[10:13], v[206:209], v[230:233], v[10:13]
	v_mfma_f32_16x16x32_bf16 v[10:13], v[202:205], v[226:229], v[10:13]
	v_mfma_f32_16x16x32_bf16 v[2:5], v[202:205], v[234:237], v[2:5]
	v_mfma_f32_16x16x32_bf16 v[2:5], v[206:209], v[238:241], v[2:5]
	v_mfma_f32_16x16x32_bf16 v[6:9], v[198:201], v[238:241], v[6:9]
	v_mfma_f32_16x16x32_bf16 v[6:9], v[194:197], v[234:237], v[6:9]
	s_barrier
	v_add_u32_e32 v166, 0x18000, v179
	ds_read_b128 v[162:165], v166
	ds_read_b128 v[182:185], v166 offset:1024
	ds_read_b128 v[186:189], v166 offset:2048
	ds_read_b128 v[190:193], v166 offset:3072
	v_add_u32_e32 v166, 0x1c000, v179
	ds_read_b128 v[194:197], v166
	ds_read_b128 v[198:201], v166 offset:1024
	ds_read_b128 v[202:205], v166 offset:2048
	ds_read_b128 v[206:209], v166 offset:3072
	s_add_i32 s29, s29, 0x80000
	s_mov_b32 m0, s43
	ds_read_b128 v[210:213], v180 offset:32768
	ds_read_b128 v[214:217], v180 offset:33792
	ds_read_b128 v[218:221], v180 offset:34816
	ds_read_b128 v[222:225], v180 offset:35840
	ds_read_b128 v[226:229], v180 offset:36864
	ds_read_b128 v[230:233], v180 offset:37888
	ds_read_b128 v[234:237], v180 offset:38912
	ds_read_b128 v[238:241], v180 offset:39936
	buffer_load_dwordx4 v1, s[4:7], s29 offen lds
	s_mov_b32 m0, s44
	s_nop 0
	buffer_load_dwordx4 v175, s[4:7], s29 offen lds
	s_waitcnt vmcnt(8)
	s_waitcnt lgkmcnt(0)
	s_barrier
	v_mfma_f32_16x16x32_bf16 v[126:129], v[162:165], v[210:213], v[126:129]
	v_mfma_f32_16x16x32_bf16 v[126:129], v[182:185], v[214:217], v[126:129]
	v_mfma_f32_16x16x32_bf16 v[122:125], v[190:193], v[214:217], v[122:125]
	v_mfma_f32_16x16x32_bf16 v[122:125], v[186:189], v[210:213], v[122:125]
	v_mfma_f32_16x16x32_bf16 v[114:117], v[186:189], v[218:221], v[114:117]
	v_mfma_f32_16x16x32_bf16 v[114:117], v[190:193], v[222:225], v[114:117]
	v_mfma_f32_16x16x32_bf16 v[118:121], v[182:185], v[222:225], v[118:121]
	v_mfma_f32_16x16x32_bf16 v[118:121], v[162:165], v[218:221], v[118:121]
	v_mfma_f32_16x16x32_bf16 v[110:113], v[162:165], v[226:229], v[110:113]
	v_mfma_f32_16x16x32_bf16 v[110:113], v[182:185], v[230:233], v[110:113]
	v_mfma_f32_16x16x32_bf16 v[106:109], v[190:193], v[230:233], v[106:109]
	v_mfma_f32_16x16x32_bf16 v[106:109], v[186:189], v[226:229], v[106:109]
	v_mfma_f32_16x16x32_bf16 v[98:101], v[186:189], v[234:237], v[98:101]
	v_mfma_f32_16x16x32_bf16 v[98:101], v[190:193], v[238:241], v[98:101]
	v_mfma_f32_16x16x32_bf16 v[102:105], v[182:185], v[238:241], v[102:105]
	v_mfma_f32_16x16x32_bf16 v[102:105], v[162:165], v[234:237], v[102:105]
	v_mfma_f32_16x16x32_bf16 v[94:97], v[194:197], v[210:213], v[94:97]
	v_mfma_f32_16x16x32_bf16 v[94:97], v[198:201], v[214:217], v[94:97]
	v_mfma_f32_16x16x32_bf16 v[90:93], v[206:209], v[214:217], v[90:93]
	v_mfma_f32_16x16x32_bf16 v[90:93], v[202:205], v[210:213], v[90:93]
	v_mfma_f32_16x16x32_bf16 v[82:85], v[202:205], v[218:221], v[82:85]
	v_mfma_f32_16x16x32_bf16 v[82:85], v[206:209], v[222:225], v[82:85]
	v_mfma_f32_16x16x32_bf16 v[86:89], v[198:201], v[222:225], v[86:89]
	v_mfma_f32_16x16x32_bf16 v[86:89], v[194:197], v[218:221], v[86:89]
	v_mfma_f32_16x16x32_bf16 v[78:81], v[194:197], v[226:229], v[78:81]
	v_mfma_f32_16x16x32_bf16 v[78:81], v[198:201], v[230:233], v[78:81]
	v_mfma_f32_16x16x32_bf16 v[74:77], v[206:209], v[230:233], v[74:77]
	v_mfma_f32_16x16x32_bf16 v[74:77], v[202:205], v[226:229], v[74:77]
	v_mfma_f32_16x16x32_bf16 v[66:69], v[202:205], v[234:237], v[66:69]
	v_mfma_f32_16x16x32_bf16 v[66:69], v[206:209], v[238:241], v[66:69]
	v_mfma_f32_16x16x32_bf16 v[70:73], v[198:201], v[238:241], v[70:73]
	v_mfma_f32_16x16x32_bf16 v[70:73], v[194:197], v[234:237], v[70:73]
	s_barrier
	s_mov_b32 m0, s49
	ds_read_b128 v[210:213], v180 offset:49152
	ds_read_b128 v[214:217], v180 offset:50176
	ds_read_b128 v[218:221], v180 offset:51200
	ds_read_b128 v[222:225], v180 offset:52224
	ds_read_b128 v[226:229], v180 offset:53248
	ds_read_b128 v[230:233], v180 offset:54272
	ds_read_b128 v[234:237], v180 offset:55296
	ds_read_b128 v[238:241], v180 offset:56320
	buffer_load_dwordx4 v174, s[8:11], s28 offen lds
	s_mov_b32 m0, s50
	s_add_i32 s27, s27, 0x80080
	buffer_load_dwordx4 v176, s[8:11], s28 offen lds
	s_mov_b32 m0, s53
	s_nop 0
	buffer_load_dwordx4 v174, s[8:11], s27 offen lds
	s_mov_b32 m0, s54
	s_nop 0
	buffer_load_dwordx4 v176, s[8:11], s27 offen lds
	s_mov_b32 m0, s51
	s_nop 0
	buffer_load_dwordx4 v1, s[4:7], s26 offen lds
	s_mov_b32 m0, s52
	s_nop 0
	buffer_load_dwordx4 v175, s[4:7], s26 offen lds
	s_waitcnt vmcnt(8)
	s_waitcnt lgkmcnt(0)
	s_barrier
	v_mfma_f32_16x16x32_bf16 v[62:65], v[162:165], v[210:213], v[62:65]
	v_mfma_f32_16x16x32_bf16 v[62:65], v[182:185], v[214:217], v[62:65]
	v_mfma_f32_16x16x32_bf16 v[58:61], v[190:193], v[214:217], v[58:61]
	v_mfma_f32_16x16x32_bf16 v[58:61], v[186:189], v[210:213], v[58:61]
	v_mfma_f32_16x16x32_bf16 v[50:53], v[186:189], v[218:221], v[50:53]
	v_mfma_f32_16x16x32_bf16 v[50:53], v[190:193], v[222:225], v[50:53]
	v_mfma_f32_16x16x32_bf16 v[54:57], v[182:185], v[222:225], v[54:57]
	v_mfma_f32_16x16x32_bf16 v[54:57], v[162:165], v[218:221], v[54:57]
	v_mfma_f32_16x16x32_bf16 v[46:49], v[162:165], v[226:229], v[46:49]
	v_mfma_f32_16x16x32_bf16 v[46:49], v[182:185], v[230:233], v[46:49]
	v_mfma_f32_16x16x32_bf16 v[42:45], v[190:193], v[230:233], v[42:45]
	v_mfma_f32_16x16x32_bf16 v[42:45], v[186:189], v[226:229], v[42:45]
	v_mfma_f32_16x16x32_bf16 v[34:37], v[186:189], v[234:237], v[34:37]
	v_mfma_f32_16x16x32_bf16 v[34:37], v[190:193], v[238:241], v[34:37]
	v_mfma_f32_16x16x32_bf16 v[38:41], v[182:185], v[238:241], v[38:41]
	v_mfma_f32_16x16x32_bf16 v[38:41], v[162:165], v[234:237], v[38:41]
	v_mfma_f32_16x16x32_bf16 v[30:33], v[194:197], v[210:213], v[30:33]
	v_mfma_f32_16x16x32_bf16 v[30:33], v[198:201], v[214:217], v[30:33]
	v_mfma_f32_16x16x32_bf16 v[26:29], v[206:209], v[214:217], v[26:29]
	v_mfma_f32_16x16x32_bf16 v[26:29], v[202:205], v[210:213], v[26:29]
	v_mfma_f32_16x16x32_bf16 v[18:21], v[202:205], v[218:221], v[18:21]
	v_mfma_f32_16x16x32_bf16 v[18:21], v[206:209], v[222:225], v[18:21]
	v_mfma_f32_16x16x32_bf16 v[22:25], v[198:201], v[222:225], v[22:25]
	v_mfma_f32_16x16x32_bf16 v[22:25], v[194:197], v[218:221], v[22:25]
	v_mfma_f32_16x16x32_bf16 v[14:17], v[194:197], v[226:229], v[14:17]
	v_mfma_f32_16x16x32_bf16 v[14:17], v[198:201], v[230:233], v[14:17]
	v_mfma_f32_16x16x32_bf16 v[10:13], v[206:209], v[230:233], v[10:13]
	v_mfma_f32_16x16x32_bf16 v[10:13], v[202:205], v[226:229], v[10:13]
	v_mfma_f32_16x16x32_bf16 v[2:5], v[202:205], v[234:237], v[2:5]
	v_mfma_f32_16x16x32_bf16 v[2:5], v[206:209], v[238:241], v[2:5]
	v_mfma_f32_16x16x32_bf16 v[6:9], v[198:201], v[238:241], v[6:9]
	v_mfma_f32_16x16x32_bf16 v[6:9], v[194:197], v[234:237], v[6:9]
	s_barrier
	s_add_i32 s10, s65, 2
	s_addk_i32 s64, 0x100
	s_cmp_gt_u32 s65, 29
	s_cbranch_scc1 .LBB0_910
	s_mov_b32 s65, s10
	s_branch .LBB0_869

.LBB0_1029:
	v_add_u32_e32 v152, 0x10000, v138
	v_add_u32_e32 v168, 0x14000, v138
	ds_read_b128 v[140:143], v152
	ds_read_b128 v[144:147], v152 offset:1024
	ds_read_b128 v[148:151], v152 offset:2048
	ds_read_b128 v[152:155], v152 offset:3072
	ds_read_b128 v[156:159], v168
	ds_read_b128 v[160:163], v168 offset:1024
	ds_read_b128 v[164:167], v168 offset:2048
	ds_read_b128 v[168:171], v168 offset:3072
	s_add_i32 s10, s30, s50
	s_add_i32 s51, s25, s50
	s_add_i32 s11, s10, 0x4000
	s_addk_i32 s51, 0x4000
	s_cmp_eq_u32 s50, 0
	s_cselect_b32 s53, s47, s11
	s_cselect_b32 s52, s48, s51
	s_or_b32 s51, s53, 0x80
	s_add_i32 s10, s10, 0x203f80
	s_mov_b32 m0, s41
	ds_read_b128 v[172:175], v139
	ds_read_b128 v[176:179], v139 offset:1024
	ds_read_b128 v[180:183], v139 offset:2048
	ds_read_b128 v[184:187], v139 offset:3072
	ds_read_b128 v[188:191], v139 offset:4096
	ds_read_b128 v[192:195], v139 offset:5120
	ds_read_b128 v[196:199], v139 offset:6144
	ds_read_b128 v[200:203], v139 offset:7168
	buffer_load_dwordx4 v134, s[4:7], s10 offen lds
	s_mov_b32 m0, s42
	s_nop 0
	buffer_load_dwordx4 v136, s[4:7], s10 offen lds
	s_waitcnt vmcnt(8)
	s_waitcnt lgkmcnt(0)
	s_barrier
	v_mfma_f32_16x16x32_bf16 v[126:129], v[140:143], v[172:175], v[126:129]
	v_mfma_f32_16x16x32_bf16 v[126:129], v[144:147], v[176:179], v[126:129]
	v_mfma_f32_16x16x32_bf16 v[122:125], v[152:155], v[176:179], v[122:125]
	v_mfma_f32_16x16x32_bf16 v[122:125], v[148:151], v[172:175], v[122:125]
	v_mfma_f32_16x16x32_bf16 v[106:109], v[148:151], v[180:183], v[106:109]
	v_mfma_f32_16x16x32_bf16 v[106:109], v[152:155], v[184:187], v[106:109]
	v_mfma_f32_16x16x32_bf16 v[114:117], v[144:147], v[184:187], v[114:117]
	v_mfma_f32_16x16x32_bf16 v[114:117], v[140:143], v[180:183], v[114:117]
	v_mfma_f32_16x16x32_bf16 v[98:101], v[140:143], v[188:191], v[98:101]
	v_mfma_f32_16x16x32_bf16 v[98:101], v[144:147], v[192:195], v[98:101]
	v_mfma_f32_16x16x32_bf16 v[90:93], v[152:155], v[192:195], v[90:93]
	v_mfma_f32_16x16x32_bf16 v[90:93], v[148:151], v[188:191], v[90:93]
	v_mfma_f32_16x16x32_bf16 v[74:77], v[148:151], v[196:199], v[74:77]
	v_mfma_f32_16x16x32_bf16 v[74:77], v[152:155], v[200:203], v[74:77]
	v_mfma_f32_16x16x32_bf16 v[82:85], v[144:147], v[200:203], v[82:85]
	v_mfma_f32_16x16x32_bf16 v[82:85], v[140:143], v[196:199], v[82:85]
	v_mfma_f32_16x16x32_bf16 v[118:121], v[156:159], v[172:175], v[118:121]
	v_mfma_f32_16x16x32_bf16 v[118:121], v[160:163], v[176:179], v[118:121]
	v_mfma_f32_16x16x32_bf16 v[110:113], v[168:171], v[176:179], v[110:113]
	v_mfma_f32_16x16x32_bf16 v[110:113], v[164:167], v[172:175], v[110:113]
	v_mfma_f32_16x16x32_bf16 v[94:97], v[164:167], v[180:183], v[94:97]
	v_mfma_f32_16x16x32_bf16 v[94:97], v[168:171], v[184:187], v[94:97]
	v_mfma_f32_16x16x32_bf16 v[102:105], v[160:163], v[184:187], v[102:105]
	v_mfma_f32_16x16x32_bf16 v[102:105], v[156:159], v[180:183], v[102:105]
	v_mfma_f32_16x16x32_bf16 v[86:89], v[156:159], v[188:191], v[86:89]
	v_mfma_f32_16x16x32_bf16 v[86:89], v[160:163], v[192:195], v[86:89]
	v_mfma_f32_16x16x32_bf16 v[78:81], v[168:171], v[192:195], v[78:81]
	v_mfma_f32_16x16x32_bf16 v[78:81], v[164:167], v[188:191], v[78:81]
	v_mfma_f32_16x16x32_bf16 v[66:69], v[164:167], v[196:199], v[66:69]
	v_mfma_f32_16x16x32_bf16 v[66:69], v[168:171], v[200:203], v[66:69]
	v_mfma_f32_16x16x32_bf16 v[70:73], v[160:163], v[200:203], v[70:73]
	v_mfma_f32_16x16x32_bf16 v[70:73], v[156:159], v[196:199], v[70:73]
	s_barrier
	s_mov_b32 m0, s24
	s_mov_b32 s10, s6
	s_mov_b32 s11, s7
	ds_read_b128 v[172:175], v139 offset:16384
	ds_read_b128 v[176:179], v139 offset:17408
	ds_read_b128 v[180:183], v139 offset:18432
	ds_read_b128 v[184:187], v139 offset:19456
	ds_read_b128 v[188:191], v139 offset:20480
	ds_read_b128 v[192:195], v139 offset:21504
	ds_read_b128 v[196:199], v139 offset:22528
	ds_read_b128 v[200:203], v139 offset:23552
	buffer_load_dwordx4 v135, s[8:11], s52 offen lds
	s_mov_b32 m0, s26
	s_add_i32 s54, s52, 0x200000
	buffer_load_dwordx4 v137, s[8:11], s52 offen lds
	s_mov_b32 m0, s27
	s_nop 0
	buffer_load_dwordx4 v135, s[8:11], s54 offen lds
	s_mov_b32 m0, s28
	s_nop 0
	buffer_load_dwordx4 v137, s[8:11], s54 offen lds
	s_mov_b32 m0, s23
	s_nop 0
	buffer_load_dwordx4 v134, s[4:7], s53 offen lds
	s_mov_b32 m0, s29
	s_nop 0
	buffer_load_dwordx4 v136, s[4:7], s53 offen lds
	s_waitcnt vmcnt(8)
	s_waitcnt lgkmcnt(0)
	s_barrier
	v_mfma_f32_16x16x32_bf16 v[62:65], v[140:143], v[172:175], v[62:65]
	v_mfma_f32_16x16x32_bf16 v[62:65], v[144:147], v[176:179], v[62:65]
	v_mfma_f32_16x16x32_bf16 v[58:61], v[152:155], v[176:179], v[58:61]
	v_mfma_f32_16x16x32_bf16 v[58:61], v[148:151], v[172:175], v[58:61]
	v_mfma_f32_16x16x32_bf16 v[42:45], v[148:151], v[180:183], v[42:45]
	v_mfma_f32_16x16x32_bf16 v[42:45], v[152:155], v[184:187], v[42:45]
	v_mfma_f32_16x16x32_bf16 v[50:53], v[144:147], v[184:187], v[50:53]
	v_mfma_f32_16x16x32_bf16 v[50:53], v[140:143], v[180:183], v[50:53]
	v_mfma_f32_16x16x32_bf16 v[34:37], v[140:143], v[188:191], v[34:37]
	v_mfma_f32_16x16x32_bf16 v[34:37], v[144:147], v[192:195], v[34:37]
	v_mfma_f32_16x16x32_bf16 v[26:29], v[152:155], v[192:195], v[26:29]
	v_mfma_f32_16x16x32_bf16 v[26:29], v[148:151], v[188:191], v[26:29]
	v_mfma_f32_16x16x32_bf16 v[10:13], v[148:151], v[196:199], v[10:13]
	v_mfma_f32_16x16x32_bf16 v[10:13], v[152:155], v[200:203], v[10:13]
	v_mfma_f32_16x16x32_bf16 v[18:21], v[144:147], v[200:203], v[18:21]
	v_mfma_f32_16x16x32_bf16 v[18:21], v[140:143], v[196:199], v[18:21]
	v_mfma_f32_16x16x32_bf16 v[54:57], v[156:159], v[172:175], v[54:57]
	v_mfma_f32_16x16x32_bf16 v[54:57], v[160:163], v[176:179], v[54:57]
	v_mfma_f32_16x16x32_bf16 v[46:49], v[168:171], v[176:179], v[46:49]
	v_mfma_f32_16x16x32_bf16 v[46:49], v[164:167], v[172:175], v[46:49]
	v_mfma_f32_16x16x32_bf16 v[30:33], v[164:167], v[180:183], v[30:33]
	v_mfma_f32_16x16x32_bf16 v[30:33], v[168:171], v[184:187], v[30:33]
	v_mfma_f32_16x16x32_bf16 v[38:41], v[160:163], v[184:187], v[38:41]
	v_mfma_f32_16x16x32_bf16 v[38:41], v[156:159], v[180:183], v[38:41]
	v_mfma_f32_16x16x32_bf16 v[22:25], v[156:159], v[188:191], v[22:25]
	v_mfma_f32_16x16x32_bf16 v[22:25], v[160:163], v[192:195], v[22:25]
	v_mfma_f32_16x16x32_bf16 v[14:17], v[168:171], v[192:195], v[14:17]
	v_mfma_f32_16x16x32_bf16 v[14:17], v[164:167], v[188:191], v[14:17]
	v_mfma_f32_16x16x32_bf16 v[2:5], v[164:167], v[196:199], v[2:5]
	v_mfma_f32_16x16x32_bf16 v[2:5], v[168:171], v[200:203], v[2:5]
	v_mfma_f32_16x16x32_bf16 v[6:9], v[160:163], v[200:203], v[6:9]
	v_mfma_f32_16x16x32_bf16 v[6:9], v[156:159], v[196:199], v[6:9]
	s_barrier
	v_add_u32_e32 v152, 0x18000, v138
	v_add_u32_e32 v168, 0x1c000, v138
	ds_read_b128 v[140:143], v152
	ds_read_b128 v[144:147], v152 offset:1024
	ds_read_b128 v[148:151], v152 offset:2048
	ds_read_b128 v[152:155], v152 offset:3072
	ds_read_b128 v[156:159], v168
	ds_read_b128 v[160:163], v168 offset:1024
	ds_read_b128 v[164:167], v168 offset:2048
	ds_read_b128 v[168:171], v168 offset:3072
	s_add_i32 s53, s53, 0x200000
	s_mov_b32 m0, s31
	ds_read_b128 v[172:175], v139 offset:32768
	ds_read_b128 v[176:179], v139 offset:33792
	ds_read_b128 v[180:183], v139 offset:34816
	ds_read_b128 v[184:187], v139 offset:35840
	ds_read_b128 v[188:191], v139 offset:36864
	ds_read_b128 v[192:195], v139 offset:37888
	ds_read_b128 v[196:199], v139 offset:38912
	ds_read_b128 v[200:203], v139 offset:39936
	buffer_load_dwordx4 v134, s[4:7], s53 offen lds
	s_mov_b32 m0, s33
	s_nop 0
	buffer_load_dwordx4 v136, s[4:7], s53 offen lds
	s_waitcnt vmcnt(8)
	s_waitcnt lgkmcnt(0)
	s_barrier
	v_mfma_f32_16x16x32_bf16 v[126:129], v[140:143], v[172:175], v[126:129]
	v_mfma_f32_16x16x32_bf16 v[126:129], v[144:147], v[176:179], v[126:129]
	v_mfma_f32_16x16x32_bf16 v[122:125], v[152:155], v[176:179], v[122:125]
	v_mfma_f32_16x16x32_bf16 v[122:125], v[148:151], v[172:175], v[122:125]
	v_mfma_f32_16x16x32_bf16 v[106:109], v[148:151], v[180:183], v[106:109]
	v_mfma_f32_16x16x32_bf16 v[106:109], v[152:155], v[184:187], v[106:109]
	v_mfma_f32_16x16x32_bf16 v[114:117], v[144:147], v[184:187], v[114:117]
	v_mfma_f32_16x16x32_bf16 v[114:117], v[140:143], v[180:183], v[114:117]
	v_mfma_f32_16x16x32_bf16 v[98:101], v[140:143], v[188:191], v[98:101]
	v_mfma_f32_16x16x32_bf16 v[98:101], v[144:147], v[192:195], v[98:101]
	v_mfma_f32_16x16x32_bf16 v[90:93], v[152:155], v[192:195], v[90:93]
	v_mfma_f32_16x16x32_bf16 v[90:93], v[148:151], v[188:191], v[90:93]
	v_mfma_f32_16x16x32_bf16 v[74:77], v[148:151], v[196:199], v[74:77]
	v_mfma_f32_16x16x32_bf16 v[74:77], v[152:155], v[200:203], v[74:77]
	v_mfma_f32_16x16x32_bf16 v[82:85], v[144:147], v[200:203], v[82:85]
	v_mfma_f32_16x16x32_bf16 v[82:85], v[140:143], v[196:199], v[82:85]
	v_mfma_f32_16x16x32_bf16 v[118:121], v[156:159], v[172:175], v[118:121]
	v_mfma_f32_16x16x32_bf16 v[118:121], v[160:163], v[176:179], v[118:121]
	v_mfma_f32_16x16x32_bf16 v[110:113], v[168:171], v[176:179], v[110:113]
	v_mfma_f32_16x16x32_bf16 v[110:113], v[164:167], v[172:175], v[110:113]
	v_mfma_f32_16x16x32_bf16 v[94:97], v[164:167], v[180:183], v[94:97]
	v_mfma_f32_16x16x32_bf16 v[94:97], v[168:171], v[184:187], v[94:97]
	v_mfma_f32_16x16x32_bf16 v[102:105], v[160:163], v[184:187], v[102:105]
	v_mfma_f32_16x16x32_bf16 v[102:105], v[156:159], v[180:183], v[102:105]
	v_mfma_f32_16x16x32_bf16 v[86:89], v[156:159], v[188:191], v[86:89]
	v_mfma_f32_16x16x32_bf16 v[86:89], v[160:163], v[192:195], v[86:89]
	v_mfma_f32_16x16x32_bf16 v[78:81], v[168:171], v[192:195], v[78:81]
	v_mfma_f32_16x16x32_bf16 v[78:81], v[164:167], v[188:191], v[78:81]
	v_mfma_f32_16x16x32_bf16 v[66:69], v[164:167], v[196:199], v[66:69]
	v_mfma_f32_16x16x32_bf16 v[66:69], v[168:171], v[200:203], v[66:69]
	v_mfma_f32_16x16x32_bf16 v[70:73], v[160:163], v[200:203], v[70:73]
	v_mfma_f32_16x16x32_bf16 v[70:73], v[156:159], v[196:199], v[70:73]
	s_barrier
	s_mov_b32 m0, s34
	s_or_b32 s53, s52, 0x80
	ds_read_b128 v[172:175], v139 offset:49152
	ds_read_b128 v[176:179], v139 offset:50176
	ds_read_b128 v[180:183], v139 offset:51200
	ds_read_b128 v[184:187], v139 offset:52224
	ds_read_b128 v[188:191], v139 offset:53248
	ds_read_b128 v[192:195], v139 offset:54272
	ds_read_b128 v[196:199], v139 offset:55296
	ds_read_b128 v[200:203], v139 offset:56320
	buffer_load_dwordx4 v135, s[8:11], s53 offen lds
	s_mov_b32 m0, s35
	s_add_i32 s52, s52, 0x200080
	buffer_load_dwordx4 v137, s[8:11], s53 offen lds
	s_mov_b32 m0, s39
	s_nop 0
	buffer_load_dwordx4 v135, s[8:11], s52 offen lds
	s_mov_b32 m0, s40
	s_nop 0
	buffer_load_dwordx4 v137, s[8:11], s52 offen lds
	s_mov_b32 m0, s37
	s_nop 0
	buffer_load_dwordx4 v134, s[4:7], s51 offen lds
	s_mov_b32 m0, s38
	s_nop 0
	buffer_load_dwordx4 v136, s[4:7], s51 offen lds
	s_waitcnt vmcnt(8)
	s_waitcnt lgkmcnt(0)
	s_barrier
	v_mfma_f32_16x16x32_bf16 v[62:65], v[140:143], v[172:175], v[62:65]
	v_mfma_f32_16x16x32_bf16 v[62:65], v[144:147], v[176:179], v[62:65]
	v_mfma_f32_16x16x32_bf16 v[58:61], v[152:155], v[176:179], v[58:61]
	v_mfma_f32_16x16x32_bf16 v[58:61], v[148:151], v[172:175], v[58:61]
	v_mfma_f32_16x16x32_bf16 v[42:45], v[148:151], v[180:183], v[42:45]
	v_mfma_f32_16x16x32_bf16 v[42:45], v[152:155], v[184:187], v[42:45]
	v_mfma_f32_16x16x32_bf16 v[50:53], v[144:147], v[184:187], v[50:53]
	v_mfma_f32_16x16x32_bf16 v[50:53], v[140:143], v[180:183], v[50:53]
	v_mfma_f32_16x16x32_bf16 v[34:37], v[140:143], v[188:191], v[34:37]
	v_mfma_f32_16x16x32_bf16 v[34:37], v[144:147], v[192:195], v[34:37]
	v_mfma_f32_16x16x32_bf16 v[26:29], v[152:155], v[192:195], v[26:29]
	v_mfma_f32_16x16x32_bf16 v[26:29], v[148:151], v[188:191], v[26:29]
	v_mfma_f32_16x16x32_bf16 v[10:13], v[148:151], v[196:199], v[10:13]
	v_mfma_f32_16x16x32_bf16 v[10:13], v[152:155], v[200:203], v[10:13]
	v_mfma_f32_16x16x32_bf16 v[18:21], v[144:147], v[200:203], v[18:21]
	v_mfma_f32_16x16x32_bf16 v[18:21], v[140:143], v[196:199], v[18:21]
	v_mfma_f32_16x16x32_bf16 v[54:57], v[156:159], v[172:175], v[54:57]
	v_mfma_f32_16x16x32_bf16 v[54:57], v[160:163], v[176:179], v[54:57]
	v_mfma_f32_16x16x32_bf16 v[46:49], v[168:171], v[176:179], v[46:49]
	v_mfma_f32_16x16x32_bf16 v[46:49], v[164:167], v[172:175], v[46:49]
	v_mfma_f32_16x16x32_bf16 v[30:33], v[164:167], v[180:183], v[30:33]
	v_mfma_f32_16x16x32_bf16 v[30:33], v[168:171], v[184:187], v[30:33]
	v_mfma_f32_16x16x32_bf16 v[38:41], v[160:163], v[184:187], v[38:41]
	v_mfma_f32_16x16x32_bf16 v[38:41], v[156:159], v[180:183], v[38:41]
	v_mfma_f32_16x16x32_bf16 v[22:25], v[156:159], v[188:191], v[22:25]
	v_mfma_f32_16x16x32_bf16 v[22:25], v[160:163], v[192:195], v[22:25]
	v_mfma_f32_16x16x32_bf16 v[14:17], v[168:171], v[192:195], v[14:17]
	v_mfma_f32_16x16x32_bf16 v[14:17], v[164:167], v[188:191], v[14:17]
	v_mfma_f32_16x16x32_bf16 v[2:5], v[164:167], v[196:199], v[2:5]
	v_mfma_f32_16x16x32_bf16 v[2:5], v[168:171], v[200:203], v[2:5]
	v_mfma_f32_16x16x32_bf16 v[6:9], v[160:163], v[200:203], v[6:9]
	v_mfma_f32_16x16x32_bf16 v[6:9], v[156:159], v[196:199], v[6:9]
	s_barrier
	s_add_i32 s49, s49, 2
	s_addk_i32 s50, 0x100
	s_cmpk_gt_u32 s49, 0x7d
	s_cbranch_scc0 .LBB0_1029
	s_andn2_b64 vcc, exec, s[2:3]
	s_cbranch_vccnz .LBB0_1021
	v_mov_b32_e32 v2, 0
	s_mov_b32 s17, s44
	s_mov_b32 s14, s45
	s_mov_b32 s25, s46
	s_mov_b32 s30, s13
	s_mov_b32 s43, s12
	v_mov_b32_e32 v3, v2
	v_mov_b32_e32 v4, v2
	v_mov_b32_e32 v5, v2
	v_mov_b32_e32 v6, v2
	v_mov_b32_e32 v7, v2
	v_mov_b32_e32 v8, v2
	v_mov_b32_e32 v9, v2
	v_mov_b32_e32 v14, v2
	v_mov_b32_e32 v15, v2
	v_mov_b32_e32 v16, v2
	v_mov_b32_e32 v17, v2
	v_mov_b32_e32 v22, v2
	v_mov_b32_e32 v23, v2
	v_mov_b32_e32 v24, v2
	v_mov_b32_e32 v25, v2
	v_mov_b32_e32 v30, v2
	v_mov_b32_e32 v31, v2
	v_mov_b32_e32 v32, v2
	v_mov_b32_e32 v33, v2
	v_mov_b32_e32 v38, v2
	v_mov_b32_e32 v39, v2
	v_mov_b32_e32 v40, v2
	v_mov_b32_e32 v41, v2
	v_mov_b32_e32 v46, v2
	v_mov_b32_e32 v47, v2
	v_mov_b32_e32 v48, v2
	v_mov_b32_e32 v49, v2
	v_mov_b32_e32 v54, v2
	v_mov_b32_e32 v55, v2
	v_mov_b32_e32 v56, v2
	v_mov_b32_e32 v57, v2
	v_mov_b32_e32 v10, v2
	v_mov_b32_e32 v11, v2
	v_mov_b32_e32 v12, v2
	v_mov_b32_e32 v13, v2
	v_mov_b32_e32 v18, v2
	v_mov_b32_e32 v19, v2
	v_mov_b32_e32 v20, v2
	v_mov_b32_e32 v21, v2
	v_mov_b32_e32 v26, v2
	v_mov_b32_e32 v27, v2
	v_mov_b32_e32 v28, v2
	v_mov_b32_e32 v29, v2
	v_mov_b32_e32 v34, v2
	v_mov_b32_e32 v35, v2
	v_mov_b32_e32 v36, v2
	v_mov_b32_e32 v37, v2
	v_mov_b32_e32 v42, v2
	v_mov_b32_e32 v43, v2
	v_mov_b32_e32 v44, v2
	v_mov_b32_e32 v45, v2
	v_mov_b32_e32 v50, v2
	v_mov_b32_e32 v51, v2
	v_mov_b32_e32 v52, v2
	v_mov_b32_e32 v53, v2
	v_mov_b32_e32 v58, v2
	v_mov_b32_e32 v59, v2
	v_mov_b32_e32 v60, v2
	v_mov_b32_e32 v61, v2
	v_mov_b32_e32 v62, v2
	v_mov_b32_e32 v63, v2
	v_mov_b32_e32 v64, v2
	v_mov_b32_e32 v65, v2
	v_mov_b32_e32 v66, v2
	v_mov_b32_e32 v67, v2
	v_mov_b32_e32 v68, v2
	v_mov_b32_e32 v69, v2
	v_mov_b32_e32 v70, v2
	v_mov_b32_e32 v71, v2
	v_mov_b32_e32 v72, v2
	v_mov_b32_e32 v73, v2
	v_mov_b32_e32 v78, v2
	v_mov_b32_e32 v79, v2
	v_mov_b32_e32 v80, v2
	v_mov_b32_e32 v81, v2
	v_mov_b32_e32 v86, v2
	v_mov_b32_e32 v87, v2
	v_mov_b32_e32 v88, v2
	v_mov_b32_e32 v89, v2
	v_mov_b32_e32 v94, v2
	v_mov_b32_e32 v95, v2
	v_mov_b32_e32 v96, v2
	v_mov_b32_e32 v97, v2
	v_mov_b32_e32 v102, v2
	v_mov_b32_e32 v103, v2
	v_mov_b32_e32 v104, v2
	v_mov_b32_e32 v105, v2
	v_mov_b32_e32 v110, v2
	v_mov_b32_e32 v111, v2
	v_mov_b32_e32 v112, v2
	v_mov_b32_e32 v113, v2
	v_mov_b32_e32 v118, v2
	v_mov_b32_e32 v119, v2
	v_mov_b32_e32 v120, v2
	v_mov_b32_e32 v121, v2
	v_mov_b32_e32 v74, v2
	v_mov_b32_e32 v75, v2
	v_mov_b32_e32 v76, v2
	v_mov_b32_e32 v77, v2
	v_mov_b32_e32 v82, v2
	v_mov_b32_e32 v83, v2
	v_mov_b32_e32 v84, v2
	v_mov_b32_e32 v85, v2
	v_mov_b32_e32 v90, v2
	v_mov_b32_e32 v91, v2
	v_mov_b32_e32 v92, v2
	v_mov_b32_e32 v93, v2
	v_mov_b32_e32 v98, v2
	v_mov_b32_e32 v99, v2
	v_mov_b32_e32 v100, v2
	v_mov_b32_e32 v101, v2
	v_mov_b32_e32 v106, v2
	v_mov_b32_e32 v107, v2
	v_mov_b32_e32 v108, v2
	v_mov_b32_e32 v109, v2
	v_mov_b32_e32 v114, v2
	v_mov_b32_e32 v115, v2
	v_mov_b32_e32 v116, v2
	v_mov_b32_e32 v117, v2
	v_mov_b32_e32 v122, v2
	v_mov_b32_e32 v123, v2
	v_mov_b32_e32 v124, v2
	v_mov_b32_e32 v125, v2
	v_mov_b32_e32 v126, v2
	v_mov_b32_e32 v127, v2
	v_mov_b32_e32 v128, v2
	v_mov_b32_e32 v129, v2
	s_branch .LBB0_1021
